# final output stores of the combine+LN phase marked nt (stream out instead of leaving dirty L2 lines for the end-of-kernel flush); on top of v6
# speedup vs baseline: 1.0007x; 1.0007x over previous
.LBB0_1515:
	s_add_i32 s2, s4, s25
	s_add_i32 s22, s2, 3
	s_ashr_i32 s23, s22, 31
	s_lshl_b64 s[2:3], s[22:23], 12
	v_lshl_add_u64 v[40:41], v[12:13], 0, s[2:3]
	v_mov_b32_e32 v154, s26
	global_load_dwordx2 v[36:37], v[40:41], off
	global_load_dwordx2 v[38:39], v[40:41], off offset:512
	global_load_dwordx2 v[34:35], v[40:41], off offset:1024
	global_load_dwordx2 v[32:33], v[40:41], off offset:1536
	global_load_dwordx2 v[30:31], v[40:41], off offset:2048
	global_load_dwordx2 v[28:29], v[40:41], off offset:2560
	global_load_dwordx2 v[26:27], v[40:41], off offset:3072
	global_load_dwordx2 v[24:25], v[40:41], off offset:3584
	ds_read_b128 v[40:43], v154
	s_waitcnt vmcnt(46)
	v_and_b32_e32 v49, 0xffff0000, v22
	v_and_b32_e32 v48, 0xffff0000, v20
	v_lshlrev_b32_e32 v57, 16, v23
	v_lshlrev_b32_e32 v56, 16, v21
	s_waitcnt lgkmcnt(0)
	v_readfirstlane_b32 s2, v40
	s_ashr_i32 s3, s2, 31
	s_lshl_b64 s[2:3], s[2:3], 11
	v_lshl_add_u64 v[44:45], v[14:15], 0, s[2:3]
	v_readfirstlane_b32 s2, v41
	s_ashr_i32 s3, s2, 31
	s_lshl_b64 s[2:3], s[2:3], 11
	v_lshl_add_u64 v[40:41], v[14:15], 0, s[2:3]
	v_readfirstlane_b32 s2, v42
	s_ashr_i32 s3, s2, 31
	s_lshl_b64 s[2:3], s[2:3], 11
	global_load_dword v144, v[44:45], off
	global_load_dword v140, v[44:45], off offset:256
	global_load_dword v136, v[44:45], off offset:512
	global_load_dword v132, v[44:45], off offset:768
	global_load_dword v128, v[44:45], off offset:1024
	global_load_dword v124, v[44:45], off offset:1280
	global_load_dword v120, v[44:45], off offset:1536
	global_load_dword v116, v[44:45], off offset:1792
	global_load_dword v145, v[40:41], off
	global_load_dword v141, v[40:41], off offset:256
	global_load_dword v137, v[40:41], off offset:512
	global_load_dword v133, v[40:41], off offset:768
	global_load_dword v129, v[40:41], off offset:1024
	global_load_dword v125, v[40:41], off offset:1280
	global_load_dword v121, v[40:41], off offset:1536
	global_load_dword v117, v[40:41], off offset:1792
	v_lshl_add_u64 v[40:41], v[14:15], 0, s[2:3]
	v_readfirstlane_b32 s2, v43
	s_ashr_i32 s3, s2, 31
	s_lshl_b64 s[2:3], s[2:3], 11
	global_load_dword v146, v[40:41], off
	global_load_dword v142, v[40:41], off offset:256
	global_load_dword v138, v[40:41], off offset:512
	global_load_dword v134, v[40:41], off offset:768
	global_load_dword v130, v[40:41], off offset:1024
	global_load_dword v126, v[40:41], off offset:1280
	global_load_dword v122, v[40:41], off offset:1536
	global_load_dword v118, v[40:41], off offset:1792
	v_lshl_add_u64 v[40:41], v[14:15], 0, s[2:3]
	global_load_dword v147, v[40:41], off
	global_load_dword v143, v[40:41], off offset:256
	global_load_dword v139, v[40:41], off offset:512
	global_load_dword v135, v[40:41], off offset:768
	global_load_dword v131, v[40:41], off offset:1024
	global_load_dword v127, v[40:41], off offset:1280
	global_load_dword v123, v[40:41], off offset:1536
	global_load_dword v119, v[40:41], off offset:1792
	v_lshlrev_b32_e32 v45, 16, v22
	v_lshlrev_b32_e32 v44, 16, v20
	v_and_b32_e32 v69, 0xffff0000, v23
	v_and_b32_e32 v68, 0xffff0000, v21
	ds_read_b128 v[40:43], v154 offset:240
	v_pk_add_f32 v[20:21], v[44:45], v[48:49]
	v_pk_add_f32 v[22:23], v[56:57], v[68:69]
	s_waitcnt vmcnt(62)
	v_lshlrev_b32_e32 v55, 16, v11
	v_lshlrev_b32_e32 v54, 16, v10
	v_and_b32_e32 v71, 0xffff0000, v11
	v_and_b32_e32 v70, 0xffff0000, v10
	v_pk_add_f32 v[20:21], v[20:21], v[22:23]
	v_pk_add_f32 v[10:11], v[54:55], v[70:71]
	v_add_f32_e32 v20, 0, v20
	v_lshlrev_b32_e32 v60, 16, v8
	v_and_b32_e32 v61, 0xffff0000, v8
	v_lshlrev_b32_e32 v62, 16, v9
	v_and_b32_e32 v63, 0xffff0000, v9
	v_lshlrev_b32_e32 v51, 16, v6
	v_and_b32_e32 v67, 0xffff0000, v6
	v_lshlrev_b32_e32 v53, 16, v7
	v_and_b32_e32 v65, 0xffff0000, v7
	v_pk_add_f32 v[6:7], v[10:11], v[10:11] op_sel:[0,1] op_sel_hi:[1,0]
	v_add_f32_e32 v50, v20, v21
	v_add_f32_e32 v52, v60, v61
	v_add_f32_e32 v64, v62, v63
	v_mov_b32_e32 v7, v67
	v_pk_add_f32 v[6:7], v[50:51], v[6:7]
	v_pk_add_f32 v[8:9], v[52:53], v[64:65]
	v_lshlrev_b32_e32 v59, 16, v5
	v_lshlrev_b32_e32 v58, 16, v4
	v_and_b32_e32 v5, 0xffff0000, v5
	v_and_b32_e32 v4, 0xffff0000, v4
	s_waitcnt lgkmcnt(0)
	v_readfirstlane_b32 s28, v42
	v_readfirstlane_b32 s27, v43
	v_pk_add_f32 v[6:7], v[6:7], v[8:9]
	v_pk_add_f32 v[42:43], v[58:59], v[4:5]
	v_readfirstlane_b32 s30, v40
	v_readfirstlane_b32 s29, v41
	v_lshlrev_b32_e32 v8, 16, v2
	v_and_b32_e32 v9, 0xffff0000, v2
	v_lshlrev_b32_e32 v10, 16, v3
	v_and_b32_e32 v11, 0xffff0000, v3
	v_lshlrev_b32_e32 v40, 16, v0
	v_and_b32_e32 v41, 0xffff0000, v0
	v_lshlrev_b32_e32 v23, 16, v1
	v_and_b32_e32 v21, 0xffff0000, v1
	v_pk_add_f32 v[0:1], v[6:7], v[6:7] op_sel:[0,1] op_sel_hi:[1,0]
	v_pk_add_f32 v[2:3], v[42:43], v[42:43] op_sel:[0,1] op_sel_hi:[1,0]
	v_add_f32_e32 v22, v8, v9
	v_add_f32_e32 v20, v10, v11
	v_mov_b32_e32 v1, v40
	v_mov_b32_e32 v3, v41
	v_pk_add_f32 v[0:1], v[0:1], v[2:3]
	v_pk_add_f32 v[2:3], v[22:23], v[20:21]
	v_cvt_pk_f32_fp8_e32 v[162:163], v113
	v_pk_add_f32 v[0:1], v[0:1], v[2:3]
	v_xor_b32_e32 v2, 1, v90
	v_add_f32_e32 v0, v0, v1
	v_and_b32_e32 v1, 64, v90
	v_add_u32_e32 v1, 64, v1
	v_cmp_lt_i32_e32 vcc, v2, v1
	v_cvt_pk_f32_fp8_sdwa v[160:161], v82 src0_sel:WORD_1
	v_mul_f32_e32 v52, s29, v98
	v_cndmask_b32_e32 v2, v90, v2, vcc
	v_lshlrev_b32_e32 v148, 2, v2
	ds_bpermute_b32 v2, v148, v0
	v_cvt_pk_f32_fp8_sdwa v[164:165], v113 src0_sel:WORD_1
	v_add_u32_e32 v155, s5, v89
	v_mul_f32_e32 v50, s28, v98
	s_waitcnt lgkmcnt(0)
	v_add_f32_e32 v0, v0, v2
	v_xor_b32_e32 v2, 2, v90
	v_cmp_lt_i32_e32 vcc, v2, v1
	s_nop 1
	v_cndmask_b32_e32 v2, v90, v2, vcc
	v_lshlrev_b32_e32 v149, 2, v2
	ds_bpermute_b32 v2, v149, v0
	s_waitcnt lgkmcnt(0)
	v_add_f32_e32 v0, v0, v2
	v_xor_b32_e32 v2, 4, v90
	v_cmp_lt_i32_e32 vcc, v2, v1
	s_nop 1
	v_cndmask_b32_e32 v2, v90, v2, vcc
	v_lshlrev_b32_e32 v150, 2, v2
	ds_bpermute_b32 v2, v150, v0
	s_waitcnt lgkmcnt(0)
	v_add_f32_e32 v0, v0, v2
	v_xor_b32_e32 v2, 8, v90
	v_cmp_lt_i32_e32 vcc, v2, v1
	s_nop 1
	v_cndmask_b32_e32 v2, v90, v2, vcc
	v_lshlrev_b32_e32 v151, 2, v2
	ds_bpermute_b32 v2, v151, v0
	s_waitcnt lgkmcnt(0)
	v_add_f32_e32 v0, v0, v2
	v_xor_b32_e32 v2, 16, v90
	v_cmp_lt_i32_e32 vcc, v2, v1
	s_nop 1
	v_cndmask_b32_e32 v2, v90, v2, vcc
	v_lshlrev_b32_e32 v152, 2, v2
	ds_bpermute_b32 v2, v152, v0
	s_waitcnt lgkmcnt(0)
	v_add_f32_e32 v0, v0, v2
	v_xor_b32_e32 v2, 32, v90
	v_cmp_lt_i32_e32 vcc, v2, v1
	s_nop 1
	v_cndmask_b32_e32 v1, v90, v2, vcc
	v_lshlrev_b32_e32 v153, 2, v1
	ds_bpermute_b32 v1, v153, v0
	s_waitcnt lgkmcnt(0)
	v_add_f32_e32 v20, v0, v1
	v_fmac_f32_e32 v68, 0xba000000, v20
	v_fmac_f32_e32 v48, 0xba000000, v20
	v_fmac_f32_e32 v69, 0xba000000, v20
	v_fmac_f32_e32 v49, 0xba000000, v20
	v_fmac_f32_e32 v56, 0xba000000, v20
	v_fmac_f32_e32 v44, 0xba000000, v20
	v_fmac_f32_e32 v57, 0xba000000, v20
	v_fmac_f32_e32 v45, 0xba000000, v20
	v_pk_mul_f32 v[0:1], v[48:49], v[48:49]
	v_pk_mul_f32 v[2:3], v[68:69], v[68:69]
	v_pk_fma_f32 v[0:1], v[44:45], v[44:45], v[0:1]
	v_pk_fma_f32 v[2:3], v[56:57], v[56:57], v[2:3]
	v_fmac_f32_e32 v70, 0xba000000, v20
	v_fmac_f32_e32 v71, 0xba000000, v20
	v_fmac_f32_e32 v55, 0xba000000, v20
	v_mov_b32_e32 v42, v44
	v_mov_b32_e32 v43, v48
	v_mov_b32_e32 v48, v57
	v_mov_b32_e32 v44, v56
	v_pk_add_f32 v[0:1], v[0:1], v[2:3]
	v_fmac_f32_e32 v54, 0xba000000, v20
	v_mov_b32_e32 v56, v55
	v_mov_b32_e32 v57, v71
	v_mov_b32_e32 v55, v70
	v_pk_add_f32 v[0:1], v[0:1], v[0:1] op_sel_hi:[0,1]
	v_pk_mul_f32 v[2:3], v[56:57], v[56:57]
	v_pk_mul_f32 v[6:7], v[54:55], v[54:55]
	v_fmac_f32_e32 v60, 0xba000000, v20
	v_mov_b32_e32 v46, v45
	v_mov_b32_e32 v47, v49
	v_mov_b32_e32 v49, v69
	v_mov_b32_e32 v45, v68
	v_pk_mov_b32 v[68:69], v[6:7], v[2:3] op_sel:[1,0]
	v_mov_b32_e32 v7, v3
	v_fmac_f32_e32 v61, 0xba000000, v20
	v_fmac_f32_e32 v62, 0xba000000, v20
	v_mul_f32_e32 v0, v60, v60
	v_pk_add_f32 v[2:3], v[68:69], v[6:7]
	v_fmac_f32_e32 v63, 0xba000000, v20
	v_pk_fma_f32 v[6:7], v[60:61], v[60:61], v[0:1] op_sel_hi:[1,1,0]
	v_mul_f32_e32 v0, v62, v62
	v_pk_add_f32 v[2:3], v[2:3], v[2:3] op_sel_hi:[0,1]
	v_pk_fma_f32 v[68:69], v[62:63], v[62:63], v[0:1] op_sel_hi:[1,1,0]
	v_fmac_f32_e32 v65, 0xba000000, v20
	v_fmac_f32_e32 v53, 0xba000000, v20
	v_fmac_f32_e32 v67, 0xba000000, v20
	v_fmac_f32_e32 v51, 0xba000000, v20
	v_mul_f32_e32 v6, v51, v51
	v_mul_f32_e32 v68, v67, v67
	v_mul_f32_e32 v2, v53, v53
	v_mul_f32_e32 v0, v65, v65
	v_pk_add_f32 v[6:7], v[6:7], v[68:69]
	v_pk_add_f32 v[0:1], v[2:3], v[0:1]
	v_fmac_f32_e32 v4, 0xba000000, v20
	v_fmac_f32_e32 v5, 0xba000000, v20
	v_fmac_f32_e32 v59, 0xba000000, v20
	v_pk_add_f32 v[0:1], v[6:7], v[0:1]
	v_fmac_f32_e32 v58, 0xba000000, v20
	v_mov_b32_e32 v68, v59
	v_mov_b32_e32 v69, v5
	v_mov_b32_e32 v59, v4
	v_pk_add_f32 v[0:1], v[0:1], v[0:1] op_sel_hi:[0,1]
	v_pk_mul_f32 v[2:3], v[68:69], v[68:69]
	v_pk_mul_f32 v[4:5], v[58:59], v[58:59]
	v_fmac_f32_e32 v8, 0xba000000, v20
	v_pk_mov_b32 v[6:7], v[4:5], v[2:3] op_sel:[1,0]
	v_mov_b32_e32 v5, v3
	v_fmac_f32_e32 v9, 0xba000000, v20
	v_fmac_f32_e32 v10, 0xba000000, v20
	v_mul_f32_e32 v0, v8, v8
	v_pk_add_f32 v[2:3], v[6:7], v[4:5]
	v_fmac_f32_e32 v11, 0xba000000, v20
	v_pk_fma_f32 v[4:5], v[8:9], v[8:9], v[0:1] op_sel_hi:[1,1,0]
	v_mul_f32_e32 v0, v10, v10
	v_pk_add_f32 v[2:3], v[2:3], v[2:3] op_sel_hi:[0,1]
	v_pk_fma_f32 v[6:7], v[10:11], v[10:11], v[0:1] op_sel_hi:[1,1,0]
	v_fmac_f32_e32 v21, 0xba000000, v20
	v_fmac_f32_e32 v23, 0xba000000, v20
	v_fmac_f32_e32 v41, 0xba000000, v20
	v_fmac_f32_e32 v40, 0xba000000, v20
	v_mul_f32_e32 v4, v40, v40
	v_mul_f32_e32 v6, v41, v41
	v_mul_f32_e32 v2, v23, v23
	v_mul_f32_e32 v0, v21, v21
	v_pk_add_f32 v[4:5], v[4:5], v[6:7]
	v_pk_add_f32 v[0:1], v[2:3], v[0:1]
	v_cvt_pk_f32_fp8_e32 v[70:71], v82
	v_pk_add_f32 v[0:1], v[4:5], v[0:1]
	v_mul_f32_e32 v82, s30, v98
	v_add_f32_e32 v0, v0, v1
	ds_bpermute_b32 v1, v148, v0
	v_pk_fma_f32 v[70:71], v[82:83], v[70:71], 0 op_sel_hi:[0,1,0]
	v_pk_fma_f32 v[70:71], v[52:53], v[162:163], v[70:71] op_sel_hi:[0,1,1]
	s_waitcnt vmcnt(55)
	v_cvt_pk_f32_fp8_e32 v[162:163], v114
	v_pk_fma_f32 v[160:161], v[82:83], v[160:161], 0 op_sel_hi:[0,1,0]
	s_waitcnt lgkmcnt(0)
	v_add_f32_e32 v0, v0, v1
	ds_bpermute_b32 v1, v149, v0
	v_pk_fma_f32 v[70:71], v[50:51], v[162:163], v[70:71] op_sel_hi:[0,1,1]
	s_waitcnt vmcnt(47)
	v_cvt_pk_f32_fp8_e32 v[162:163], v115
	v_pk_fma_f32 v[160:161], v[52:53], v[164:165], v[160:161] op_sel_hi:[0,1,1]
	v_cvt_pk_f32_fp8_sdwa v[164:165], v114 src0_sel:WORD_1
	s_waitcnt lgkmcnt(0)
	v_add_f32_e32 v0, v0, v1
	ds_bpermute_b32 v1, v150, v0
	v_cvt_pk_f32_fp8_sdwa v[114:115], v115 src0_sel:WORD_1
	v_mul_f32_e32 v20, s27, v98
	v_pk_fma_f32 v[70:71], v[20:21], v[162:163], v[70:71] op_sel_hi:[0,1,1]
	v_pk_fma_f32 v[160:161], v[50:51], v[164:165], v[160:161] op_sel_hi:[0,1,1]
	s_waitcnt lgkmcnt(0)
	v_add_f32_e32 v0, v0, v1
	ds_bpermute_b32 v1, v151, v0
	v_pk_fma_f32 v[114:115], v[20:21], v[114:115], v[160:161] op_sel_hi:[0,1,1]
	v_cvt_pk_f32_fp8_e32 v[160:161], v110
	v_cvt_pk_f32_fp8_sdwa v[162:163], v110 src0_sel:WORD_1
	v_mov_b32_e32 v64, v53
	s_waitcnt lgkmcnt(0)
	v_add_f32_e32 v0, v0, v1
	ds_bpermute_b32 v1, v152, v0
	s_waitcnt vmcnt(23)
	v_cvt_pk_f32_fp8_e32 v[164:165], v145
	s_waitcnt lgkmcnt(0)
	v_add_f32_e32 v0, v0, v1
	ds_bpermute_b32 v1, v153, v0
	s_waitcnt lgkmcnt(0)
	v_add_f32_e32 v0, v0, v1
	v_fmamk_f32 v0, v0, 0x3a000000, v91
	v_cmp_gt_f32_e32 vcc, s7, v0
	v_mul_f32_e32 v1, 0x4f800000, v0
	s_nop 0
	v_cndmask_b32_e32 v0, v0, v1, vcc
	v_sqrt_f32_e32 v1, v0
	s_nop 0
	v_add_u32_e32 v2, -1, v1
	v_fma_f32 v3, -v2, v1, v0
	v_cmp_ge_f32_e64 s[2:3], 0, v3
	v_add_u32_e32 v3, 1, v1
	s_nop 0
	v_cndmask_b32_e64 v2, v1, v2, s[2:3]
	v_fma_f32 v1, -v3, v1, v0
	v_cmp_lt_f32_e64 s[2:3], 0, v1
	s_nop 1
	v_cndmask_b32_e64 v1, v2, v3, s[2:3]
	v_mul_f32_e32 v2, 0x37800000, v1
	v_cndmask_b32_e32 v1, v1, v2, vcc
	v_cmp_class_f32_e32 vcc, v0, v92
	s_nop 1
	v_cndmask_b32_e32 v0, v1, v0, vcc
	v_div_scale_f32 v1, s[2:3], v0, v0, 1.0
	v_rcp_f32_e32 v2, v1
	s_nop 0
	v_fma_f32 v3, -v1, v2, 1.0
	v_fmac_f32_e32 v2, v3, v2
	v_div_scale_f32 v3, vcc, 1.0, v0, 1.0
	v_mul_f32_e32 v4, v3, v2
	v_fma_f32 v5, -v1, v4, v3
	v_fmac_f32_e32 v4, v5, v2
	v_fma_f32 v1, -v1, v4, v3
	v_div_fmas_f32 v1, v1, v2, v4
	v_div_fixup_f32 v22, v1, v0, 1.0
	ds_read_b128 v[0:3], v89
	ds_read_b128 v[4:7], v89 offset:8192
	ds_read_b128 v[156:159], v155 offset:32768
	v_pk_mul_f32 v[42:43], v[42:43], v[22:23] op_sel_hi:[1,0]
	v_pk_mul_f32 v[44:45], v[44:45], v[22:23] op_sel_hi:[1,0]
	v_pk_mul_f32 v[48:49], v[48:49], v[22:23] op_sel_hi:[1,0]
	s_waitcnt lgkmcnt(1)
	v_pk_fma_f32 v[0:1], v[0:1], v[42:43], v[4:5]
	v_pk_fma_f32 v[2:3], v[2:3], v[44:45], v[6:7]
	v_pk_mul_f32 v[0:1], v[0:1], s[18:19] op_sel_hi:[1,0]
	v_pk_mul_f32 v[2:3], v[2:3], s[18:19] op_sel_hi:[1,0]
	s_waitcnt lgkmcnt(0)
	v_pk_fma_f32 v[44:45], v[156:157], v[70:71], v[0:1]
	v_cvt_pk_f32_fp8_e32 v[70:71], v109
	v_pk_fma_f32 v[42:43], v[158:159], v[114:115], v[2:3]
	v_cvt_pk_f32_fp8_sdwa v[114:115], v109 src0_sel:WORD_1
	ds_read_b128 v[0:3], v89 offset:1024
	ds_read_b128 v[4:7], v89 offset:9216
	ds_read_b128 v[156:159], v155 offset:33792
	v_pk_fma_f32 v[70:71], v[82:83], v[70:71], 0 op_sel_hi:[0,1,0]
	v_pk_fma_f32 v[70:71], v[52:53], v[160:161], v[70:71] op_sel_hi:[0,1,1]
	v_cvt_pk_f32_fp8_e32 v[160:161], v111
	v_cvt_pk_f32_fp8_sdwa v[110:111], v111 src0_sel:WORD_1
	v_pk_fma_f32 v[114:115], v[82:83], v[114:115], 0 op_sel_hi:[0,1,0]
	v_pk_fma_f32 v[114:115], v[52:53], v[162:163], v[114:115] op_sel_hi:[0,1,1]
	v_pk_fma_f32 v[70:71], v[50:51], v[160:161], v[70:71] op_sel_hi:[0,1,1]
	v_pk_fma_f32 v[110:111], v[50:51], v[110:111], v[114:115] op_sel_hi:[0,1,1]
	v_cvt_pk_f32_fp8_e32 v[114:115], v112
	v_pk_mul_f32 v[46:47], v[46:47], v[22:23] op_sel_hi:[1,0]
	s_waitcnt lgkmcnt(1)
	v_pk_fma_f32 v[2:3], v[2:3], v[48:49], v[6:7]
	v_cvt_pk_f32_fp8_e32 v[6:7], v105
	v_cvt_pk_f32_fp8_sdwa v[112:113], v112 src0_sel:WORD_1
	v_pk_fma_f32 v[70:71], v[20:21], v[114:115], v[70:71] op_sel_hi:[0,1,1]
	v_pk_fma_f32 v[0:1], v[0:1], v[46:47], v[4:5]
	v_cvt_pk_f32_fp8_e32 v[114:115], v106
	v_pk_mul_f32 v[0:1], v[0:1], s[18:19] op_sel_hi:[1,0]
	v_pk_fma_f32 v[6:7], v[82:83], v[6:7], 0 op_sel_hi:[0,1,0]
	s_waitcnt lgkmcnt(0)
	v_pk_fma_f32 v[48:49], v[156:157], v[70:71], v[0:1]
	v_cvt_pk_f32_fp8_sdwa v[70:71], v105 src0_sel:WORD_1
	v_cvt_pk_f32_fp8_sdwa v[160:161], v106 src0_sel:WORD_1
	v_pk_fma_f32 v[110:111], v[20:21], v[112:113], v[110:111] op_sel_hi:[0,1,1]
	v_pk_mul_f32 v[2:3], v[2:3], s[18:19] op_sel_hi:[1,0]
	v_pk_fma_f32 v[6:7], v[52:53], v[114:115], v[6:7] op_sel_hi:[0,1,1]
	v_cvt_pk_f32_fp8_e32 v[114:115], v107
	v_cvt_pk_f32_fp8_sdwa v[106:107], v107 src0_sel:WORD_1
	v_pk_fma_f32 v[46:47], v[158:159], v[110:111], v[2:3]
	v_mov_b32_e32 v0, v48
	v_mov_b32_e32 v1, v44
	v_mov_b32_e32 v2, v49
	v_mov_b32_e32 v3, v45
	v_pk_add_f32 v[0:1], v[0:1], v[2:3]
	v_mov_b32_e32 v2, v46
	v_mov_b32_e32 v3, v42
	v_mov_b32_e32 v4, v47
	v_mov_b32_e32 v5, v43
	v_pk_fma_f32 v[70:71], v[82:83], v[70:71], 0 op_sel_hi:[0,1,0]
	v_pk_add_f32 v[2:3], v[2:3], v[4:5]
	v_pk_fma_f32 v[70:71], v[52:53], v[160:161], v[70:71] op_sel_hi:[0,1,1]
	v_pk_add_f32 v[0:1], v[0:1], v[2:3]
	ds_read_b128 v[2:5], v89 offset:2048
	ds_read_b128 v[110:113], v89 offset:10240
	ds_read_b128 v[156:159], v155 offset:34816
	v_pk_fma_f32 v[70:71], v[50:51], v[106:107], v[70:71] op_sel_hi:[0,1,1]
	v_cvt_pk_f32_fp8_e32 v[106:107], v108
	v_cvt_pk_f32_fp8_sdwa v[108:109], v108 src0_sel:WORD_1
	v_pk_fma_f32 v[6:7], v[50:51], v[114:115], v[6:7] op_sel_hi:[0,1,1]
	v_pk_mul_f32 v[54:55], v[54:55], v[22:23] op_sel_hi:[1,0]
	v_pk_fma_f32 v[6:7], v[20:21], v[106:107], v[6:7] op_sel_hi:[0,1,1]
	v_pk_fma_f32 v[70:71], v[20:21], v[108:109], v[70:71] op_sel_hi:[0,1,1]
	s_waitcnt lgkmcnt(1)
	v_pk_fma_f32 v[2:3], v[2:3], v[54:55], v[110:111]
	s_waitcnt lgkmcnt(0)
	v_pk_mul_f32 v[54:55], v[158:159], v[70:71]
	v_cvt_pk_f32_fp8_e32 v[70:71], v101
	v_pk_mul_f32 v[6:7], v[156:157], v[6:7]
	v_cvt_pk_f32_fp8_e32 v[156:157], v102
	v_cvt_pk_f32_fp8_sdwa v[114:115], v101 src0_sel:WORD_1
	v_pk_mul_f32 v[56:57], v[56:57], v[22:23] op_sel_hi:[1,0]
	v_pk_fma_f32 v[70:71], v[82:83], v[70:71], 0 op_sel_hi:[0,1,0]
	v_cvt_pk_f32_fp8_sdwa v[158:159], v102 src0_sel:WORD_1
	v_pk_fma_f32 v[4:5], v[4:5], v[56:57], v[112:113]
	v_pk_fma_f32 v[70:71], v[52:53], v[156:157], v[70:71] op_sel_hi:[0,1,1]
	v_cvt_pk_f32_fp8_e32 v[156:157], v103
	v_cvt_pk_f32_fp8_sdwa v[102:103], v103 src0_sel:WORD_1
	v_pk_fma_f32 v[54:55], v[4:5], s[18:19], v[54:55] op_sel_hi:[1,0,1]
	v_pk_fma_f32 v[56:57], v[2:3], s[18:19], v[6:7] op_sel_hi:[1,0,1]
	v_mov_b32_e32 v5, v55
	v_pk_mov_b32 v[2:3], v[56:57], v[54:55] op_sel:[1,0]
	v_mov_b32_e32 v4, v56
	v_pk_fma_f32 v[114:115], v[82:83], v[114:115], 0 op_sel_hi:[0,1,0]
	v_pk_add_f32 v[2:3], v[2:3], v[4:5]
	v_pk_fma_f32 v[114:115], v[52:53], v[158:159], v[114:115] op_sel_hi:[0,1,1]
	v_pk_add_f32 v[6:7], v[2:3], v[2:3] op_sel:[0,1] op_sel_hi:[1,0]
	ds_read_b128 v[2:5], v89 offset:3072
	ds_read_b128 v[106:109], v89 offset:11264
	ds_read_b128 v[110:113], v155 offset:35840
	v_pk_fma_f32 v[102:103], v[50:51], v[102:103], v[114:115] op_sel_hi:[0,1,1]
	v_cvt_pk_f32_fp8_e32 v[114:115], v104
	v_cvt_pk_f32_fp8_sdwa v[104:105], v104 src0_sel:WORD_1
	v_pk_mul_f32 v[60:61], v[60:61], v[22:23] op_sel_hi:[1,0]
	v_pk_fma_f32 v[70:71], v[50:51], v[156:157], v[70:71] op_sel_hi:[0,1,1]
	s_waitcnt lgkmcnt(1)
	v_pk_fma_f32 v[2:3], v[60:61], v[2:3], v[106:107]
	v_pk_fma_f32 v[102:103], v[20:21], v[104:105], v[102:103] op_sel_hi:[0,1,1]
	s_waitcnt lgkmcnt(0)
	v_pk_mul_f32 v[60:61], v[112:113], v[102:103]
	v_cvt_pk_f32_fp8_e32 v[112:113], v66
	v_cvt_pk_f32_fp8_e32 v[156:157], v84
	v_pk_fma_f32 v[70:71], v[20:21], v[114:115], v[70:71] op_sel_hi:[0,1,1]
	v_cvt_pk_f32_fp8_sdwa v[114:115], v66 src0_sel:WORD_1
	v_pk_fma_f32 v[112:113], v[82:83], v[112:113], 0 op_sel_hi:[0,1,0]
	v_cvt_pk_f32_fp8_sdwa v[158:159], v84 src0_sel:WORD_1
	v_pk_fma_f32 v[112:113], v[52:53], v[156:157], v[112:113] op_sel_hi:[0,1,1]
	v_cvt_pk_f32_fp8_e32 v[156:157], v85
	v_cvt_pk_f32_fp8_sdwa v[84:85], v85 src0_sel:WORD_1
	v_pk_mul_f32 v[62:63], v[62:63], v[22:23] op_sel_hi:[1,0]
	v_pk_fma_f32 v[114:115], v[82:83], v[114:115], 0 op_sel_hi:[0,1,0]
	v_pk_fma_f32 v[4:5], v[62:63], v[4:5], v[108:109]
	v_pk_mul_f32 v[62:63], v[110:111], v[70:71]
	v_pk_fma_f32 v[114:115], v[52:53], v[158:159], v[114:115] op_sel_hi:[0,1,1]
	v_pk_fma_f32 v[60:61], v[4:5], s[18:19], v[60:61] op_sel_hi:[1,0,1]
	v_pk_fma_f32 v[62:63], v[2:3], s[18:19], v[62:63] op_sel_hi:[1,0,1]
	ds_read_b128 v[2:5], v89 offset:4096
	ds_read_b128 v[102:105], v89 offset:12288
	ds_read_b128 v[106:109], v155 offset:36864
	v_pk_fma_f32 v[84:85], v[50:51], v[84:85], v[114:115] op_sel_hi:[0,1,1]
	v_cvt_pk_f32_fp8_e32 v[114:115], v100
	v_cvt_pk_f32_fp8_sdwa v[100:101], v100 src0_sel:WORD_1
	v_pk_fma_f32 v[112:113], v[50:51], v[156:157], v[112:113] op_sel_hi:[0,1,1]
	v_pk_mul_f32 v[64:65], v[64:65], v[22:23] op_sel_hi:[1,0]
	v_mov_b32_e32 v66, v51
	v_pk_fma_f32 v[112:113], v[20:21], v[114:115], v[112:113] op_sel_hi:[0,1,1]
	v_pk_fma_f32 v[84:85], v[20:21], v[100:101], v[84:85] op_sel_hi:[0,1,1]
	v_pk_mul_f32 v[66:67], v[66:67], v[22:23] op_sel_hi:[1,0]
	s_waitcnt lgkmcnt(1)
	v_pk_fma_f32 v[4:5], v[64:65], v[4:5], v[104:105]
	v_cvt_pk_f32_fp8_sdwa v[104:105], v76 src0_sel:WORD_1
	v_pk_fma_f32 v[2:3], v[66:67], v[2:3], v[102:103]
	s_waitcnt lgkmcnt(0)
	v_pk_mul_f32 v[64:65], v[108:109], v[84:85]
	v_pk_mul_f32 v[66:67], v[106:107], v[112:113]
	v_cvt_pk_f32_fp8_e32 v[84:85], v76
	v_cvt_pk_f32_fp8_e32 v[106:107], v77
	v_cvt_pk_f32_fp8_sdwa v[76:77], v77 src0_sel:WORD_1
	v_pk_fma_f32 v[104:105], v[82:83], v[104:105], 0 op_sel_hi:[0,1,0]
	v_add_f32_e32 v1, 0, v1
	v_pk_fma_f32 v[64:65], v[4:5], s[18:19], v[64:65] op_sel_hi:[1,0,1]
	v_pk_fma_f32 v[66:67], v[2:3], s[18:19], v[66:67] op_sel_hi:[1,0,1]
	v_pk_fma_f32 v[84:85], v[82:83], v[84:85], 0 op_sel_hi:[0,1,0]
	v_pk_fma_f32 v[76:77], v[52:53], v[76:77], v[104:105] op_sel_hi:[0,1,1]
	v_cvt_pk_f32_fp8_e32 v[104:105], v78
	v_add_f32_e32 v0, v0, v1
	v_add_f32_e32 v70, v62, v63
	v_add_f32_e32 v110, v60, v61
	v_mov_b32_e32 v1, v66
	v_mov_b32_e32 v7, v67
	v_mov_b32_e32 v71, v64
	v_mov_b32_e32 v111, v65
	v_pk_fma_f32 v[84:85], v[52:53], v[106:107], v[84:85] op_sel_hi:[0,1,1]
	v_cvt_pk_f32_fp8_sdwa v[106:107], v78 src0_sel:WORD_1
	v_pk_add_f32 v[0:1], v[0:1], v[6:7]
	v_pk_add_f32 v[2:3], v[70:71], v[110:111]
	v_pk_fma_f32 v[84:85], v[50:51], v[104:105], v[84:85] op_sel_hi:[0,1,1]
	v_pk_add_f32 v[0:1], v[0:1], v[2:3]
	v_cvt_pk_f32_fp8_e32 v[104:105], v80
	v_pk_add_f32 v[70:71], v[0:1], v[0:1] op_sel:[0,1] op_sel_hi:[1,0]
	ds_read_b128 v[0:3], v89 offset:5120
	ds_read_b128 v[4:7], v89 offset:13312
	ds_read_b128 v[100:103], v155 offset:37888
	v_pk_fma_f32 v[76:77], v[50:51], v[106:107], v[76:77] op_sel_hi:[0,1,1]
	v_cvt_pk_f32_fp8_sdwa v[106:107], v80 src0_sel:WORD_1
	v_pk_fma_f32 v[84:85], v[20:21], v[104:105], v[84:85] op_sel_hi:[0,1,1]
	v_pk_mul_f32 v[68:69], v[68:69], v[22:23] op_sel_hi:[1,0]
	v_cvt_pk_f32_fp8_sdwa v[104:105], v72 src0_sel:WORD_1
	v_pk_fma_f32 v[76:77], v[20:21], v[106:107], v[76:77] op_sel_hi:[0,1,1]
	s_waitcnt lgkmcnt(1)
	v_pk_fma_f32 v[2:3], v[68:69], v[2:3], v[6:7]
	s_waitcnt lgkmcnt(0)
	v_pk_mul_f32 v[6:7], v[100:101], v[84:85]
	v_cvt_pk_f32_fp8_e32 v[84:85], v72
	v_cvt_pk_f32_fp8_e32 v[106:107], v73
	v_cvt_pk_f32_fp8_sdwa v[72:73], v73 src0_sel:WORD_1
	v_pk_mul_f32 v[58:59], v[58:59], v[22:23] op_sel_hi:[1,0]
	v_pk_fma_f32 v[104:105], v[82:83], v[104:105], 0 op_sel_hi:[0,1,0]
	v_pk_fma_f32 v[0:1], v[58:59], v[0:1], v[4:5]
	v_pk_mul_f32 v[4:5], v[102:103], v[76:77]
	v_pk_fma_f32 v[72:73], v[52:53], v[72:73], v[104:105] op_sel_hi:[0,1,1]
	v_cvt_pk_f32_fp8_e32 v[104:105], v74
	v_pk_fma_f32 v[58:59], v[2:3], s[18:19], v[4:5] op_sel_hi:[1,0,1]
	v_pk_fma_f32 v[68:69], v[0:1], s[18:19], v[6:7] op_sel_hi:[1,0,1]
	v_mov_b32_e32 v3, v59
	v_pk_mov_b32 v[0:1], v[68:69], v[58:59] op_sel:[1,0]
	v_mov_b32_e32 v2, v68
	v_pk_fma_f32 v[84:85], v[82:83], v[84:85], 0 op_sel_hi:[0,1,0]
	v_pk_add_f32 v[0:1], v[0:1], v[2:3]
	v_pk_fma_f32 v[84:85], v[52:53], v[106:107], v[84:85] op_sel_hi:[0,1,1]
	v_pk_add_f32 v[76:77], v[0:1], v[0:1] op_sel:[0,1] op_sel_hi:[1,0]
	ds_read_b128 v[0:3], v89 offset:6144
	ds_read_b128 v[4:7], v89 offset:14336
	ds_read_b128 v[100:103], v155 offset:38912
	v_pk_fma_f32 v[84:85], v[50:51], v[104:105], v[84:85] op_sel_hi:[0,1,1]
	v_cvt_pk_f32_fp8_e32 v[104:105], v75
	v_cvt_pk_f32_fp8_sdwa v[106:107], v74 src0_sel:WORD_1
	v_cvt_pk_f32_fp8_sdwa v[74:75], v75 src0_sel:WORD_1
	v_pk_mul_f32 v[10:11], v[10:11], v[22:23] op_sel_hi:[1,0]
	v_pk_fma_f32 v[84:85], v[20:21], v[104:105], v[84:85] op_sel_hi:[0,1,1]
	s_waitcnt lgkmcnt(1)
	v_pk_fma_f32 v[2:3], v[10:11], v[2:3], v[6:7]
	s_waitcnt lgkmcnt(0)
	v_pk_mul_f32 v[6:7], v[100:101], v[84:85]
	v_cvt_pk_f32_fp8_e32 v[100:101], v83
	v_cvt_pk_f32_fp8_sdwa v[84:85], v83 src0_sel:WORD_1
	v_pk_fma_f32 v[72:73], v[50:51], v[106:107], v[72:73] op_sel_hi:[0,1,1]
	v_pk_fma_f32 v[72:73], v[20:21], v[74:75], v[72:73] op_sel_hi:[0,1,1]
	v_pk_mul_f32 v[8:9], v[8:9], v[22:23] op_sel_hi:[1,0]
	v_pk_fma_f32 v[84:85], v[82:83], v[84:85], 0 op_sel_hi:[0,1,0]
	v_pk_fma_f32 v[0:1], v[8:9], v[0:1], v[4:5]
	v_pk_mul_f32 v[4:5], v[102:103], v[72:73]
	v_pk_fma_f32 v[82:83], v[82:83], v[100:101], 0 op_sel_hi:[0,1,0]
	v_cvt_pk_f32_fp8_e32 v[100:101], v99
	v_cvt_pk_f32_fp8_sdwa v[102:103], v99 src0_sel:WORD_1
	v_pk_fma_f32 v[72:73], v[2:3], s[18:19], v[4:5] op_sel_hi:[1,0,1]
	v_pk_fma_f32 v[74:75], v[0:1], s[18:19], v[6:7] op_sel_hi:[1,0,1]
	v_pk_fma_f32 v[82:83], v[52:53], v[100:101], v[82:83] op_sel_hi:[0,1,1]
	v_pk_fma_f32 v[52:53], v[52:53], v[102:103], v[84:85] op_sel_hi:[0,1,1]
	v_cvt_pk_f32_fp8_e32 v[84:85], v81
	v_cvt_pk_f32_fp8_sdwa v[100:101], v81 src0_sel:WORD_1
	ds_read_b128 v[0:3], v89 offset:7168
	ds_read_b128 v[8:11], v89 offset:15360
	ds_read_b128 v[4:7], v155 offset:39936
	v_add_f32_e32 v78, v74, v75
	v_add_f32_e32 v80, v72, v73
	v_pk_fma_f32 v[52:53], v[50:51], v[100:101], v[52:53] op_sel_hi:[0,1,1]
	v_pk_fma_f32 v[50:51], v[50:51], v[84:85], v[82:83] op_sel_hi:[0,1,1]
	v_cvt_pk_f32_fp8_e32 v[82:83], v79
	v_cvt_pk_f32_fp8_sdwa v[84:85], v79 src0_sel:WORD_1
	v_pk_fma_f32 v[50:51], v[20:21], v[82:83], v[50:51] op_sel_hi:[0,1,1]
	v_pk_fma_f32 v[52:53], v[20:21], v[84:85], v[52:53] op_sel_hi:[0,1,1]
	v_mov_b32_e32 v20, v23
	v_pk_mul_f32 v[20:21], v[20:21], v[22:23] op_sel_hi:[1,0]
	v_pk_mul_f32 v[22:23], v[40:41], v[22:23] op_sel_hi:[1,0]
	s_waitcnt lgkmcnt(1)
	v_pk_fma_f32 v[2:3], v[20:21], v[2:3], v[10:11]
	v_pk_fma_f32 v[0:1], v[22:23], v[0:1], v[8:9]
	s_waitcnt lgkmcnt(0)
	v_pk_mul_f32 v[6:7], v[6:7], v[52:53]
	v_pk_mul_f32 v[4:5], v[4:5], v[50:51]
	v_pk_fma_f32 v[8:9], v[2:3], s[18:19], v[6:7] op_sel_hi:[1,0,1]
	v_pk_fma_f32 v[10:11], v[0:1], s[18:19], v[4:5] op_sel_hi:[1,0,1]
	v_mov_b32_e32 v79, v8
	v_mov_b32_e32 v71, v10
	v_mov_b32_e32 v77, v11
	v_mov_b32_e32 v81, v9
	v_pk_add_f32 v[0:1], v[70:71], v[76:77]
	v_pk_add_f32 v[2:3], v[78:79], v[80:81]
	v_and_b32_e32 v71, 0xffff0000, v39
	v_pk_add_f32 v[0:1], v[0:1], v[2:3]
	v_and_b32_e32 v70, 0xffff0000, v37
	v_add_f32_e32 v0, v0, v1
	ds_bpermute_b32 v1, v148, v0
	v_lshlrev_b32_e32 v50, 16, v27
	v_and_b32_e32 v51, 0xffff0000, v27
	v_lshlrev_b32_e32 v52, 16, v24
	v_and_b32_e32 v53, 0xffff0000, v24
	s_waitcnt lgkmcnt(0)
	v_add_f32_e32 v0, v0, v1
	ds_bpermute_b32 v1, v149, v0
	s_waitcnt lgkmcnt(0)
	v_add_f32_e32 v0, v0, v1
	ds_bpermute_b32 v1, v150, v0
	s_waitcnt lgkmcnt(0)
	v_add_f32_e32 v0, v0, v1
	ds_bpermute_b32 v1, v151, v0
	s_waitcnt lgkmcnt(0)
	v_add_f32_e32 v0, v0, v1
	ds_bpermute_b32 v1, v152, v0
	s_waitcnt lgkmcnt(0)
	v_add_f32_e32 v0, v0, v1
	ds_bpermute_b32 v1, v153, v0
	s_waitcnt lgkmcnt(0)
	v_add_f32_e32 v20, v0, v1
	v_fmamk_f32 v45, v20, 0xba000000, v45
	v_fmamk_f32 v49, v20, 0xba000000, v49
	v_fmamk_f32 v43, v20, 0xba000000, v43
	v_fmac_f32_e32 v44, 0xba000000, v20
	v_fmamk_f32 v47, v20, 0xba000000, v47
	v_fmac_f32_e32 v48, 0xba000000, v20
	v_mov_b32_e32 v2, v45
	v_mov_b32_e32 v3, v49
	v_fmac_f32_e32 v42, 0xba000000, v20
	v_fmac_f32_e32 v46, 0xba000000, v20
	v_mov_b32_e32 v0, v44
	v_mov_b32_e32 v1, v48
	v_pk_mul_f32 v[2:3], v[2:3], v[2:3]
	v_mov_b32_e32 v4, v43
	v_mov_b32_e32 v5, v47
	v_pk_fma_f32 v[0:1], v[0:1], v[0:1], v[2:3]
	v_mov_b32_e32 v2, v42
	v_mov_b32_e32 v3, v46
	v_pk_mul_f32 v[4:5], v[4:5], v[4:5]
	v_fmamk_f32 v57, v20, 0xba000000, v57
	v_pk_fma_f32 v[2:3], v[2:3], v[2:3], v[4:5]
	v_fmac_f32_e32 v56, 0xba000000, v20
	v_pk_add_f32 v[0:1], v[0:1], v[2:3]
	v_fmamk_f32 v55, v20, 0xba000000, v55
	v_fmac_f32_e32 v54, 0xba000000, v20
	v_pk_add_f32 v[0:1], v[0:1], v[0:1] op_sel_hi:[0,1]
	v_pk_mul_f32 v[2:3], v[54:55], v[54:55]
	v_pk_mul_f32 v[4:5], v[56:57], v[56:57]
	v_fmac_f32_e32 v62, 0xba000000, v20
	v_pk_mov_b32 v[6:7], v[4:5], v[2:3] op_sel:[1,0]
	v_mov_b32_e32 v5, v3
	v_fmamk_f32 v63, v20, 0xba000000, v63
	v_fmac_f32_e32 v60, 0xba000000, v20
	v_mul_f32_e32 v0, v62, v62
	v_pk_add_f32 v[2:3], v[6:7], v[4:5]
	v_fmamk_f32 v61, v20, 0xba000000, v61
	v_pk_fma_f32 v[4:5], v[62:63], v[62:63], v[0:1] op_sel_hi:[1,1,0]
	v_mul_f32_e32 v0, v60, v60
	v_pk_add_f32 v[2:3], v[2:3], v[2:3] op_sel_hi:[0,1]
	v_pk_fma_f32 v[6:7], v[60:61], v[60:61], v[0:1] op_sel_hi:[1,1,0]
	v_fmamk_f32 v65, v20, 0xba000000, v65
	v_fmac_f32_e32 v64, 0xba000000, v20
	v_fmamk_f32 v67, v20, 0xba000000, v67
	v_fmac_f32_e32 v66, 0xba000000, v20
	v_mul_f32_e32 v4, v66, v66
	v_mul_f32_e32 v6, v67, v67
	v_mul_f32_e32 v2, v64, v64
	v_mul_f32_e32 v0, v65, v65
	v_pk_add_f32 v[4:5], v[4:5], v[6:7]
	v_pk_add_f32 v[0:1], v[2:3], v[0:1]
	v_fmamk_f32 v69, v20, 0xba000000, v69
	v_pk_add_f32 v[0:1], v[4:5], v[0:1]
	v_fmac_f32_e32 v68, 0xba000000, v20
	v_fmamk_f32 v59, v20, 0xba000000, v59
	v_fmac_f32_e32 v58, 0xba000000, v20
	v_pk_add_f32 v[0:1], v[0:1], v[0:1] op_sel_hi:[0,1]
	v_pk_mul_f32 v[2:3], v[58:59], v[58:59]
	v_pk_mul_f32 v[4:5], v[68:69], v[68:69]
	v_fmac_f32_e32 v74, 0xba000000, v20
	v_pk_mov_b32 v[6:7], v[4:5], v[2:3] op_sel:[1,0]
	v_mov_b32_e32 v5, v3
	v_fmamk_f32 v75, v20, 0xba000000, v75
	v_fmac_f32_e32 v72, 0xba000000, v20
	v_mul_f32_e32 v0, v74, v74
	v_pk_add_f32 v[2:3], v[6:7], v[4:5]
	v_fmamk_f32 v73, v20, 0xba000000, v73
	v_pk_fma_f32 v[4:5], v[74:75], v[74:75], v[0:1] op_sel_hi:[1,1,0]
	v_mul_f32_e32 v0, v72, v72
	v_pk_add_f32 v[2:3], v[2:3], v[2:3] op_sel_hi:[0,1]
	v_pk_fma_f32 v[6:7], v[72:73], v[72:73], v[0:1] op_sel_hi:[1,1,0]
	v_fmamk_f32 v9, v20, 0xba000000, v9
	v_fmac_f32_e32 v8, 0xba000000, v20
	v_fmamk_f32 v11, v20, 0xba000000, v11
	v_fmac_f32_e32 v10, 0xba000000, v20
	v_mul_f32_e32 v4, v10, v10
	v_mul_f32_e32 v6, v11, v11
	v_mul_f32_e32 v2, v8, v8
	v_mul_f32_e32 v0, v9, v9
	v_pk_add_f32 v[4:5], v[4:5], v[6:7]
	v_pk_add_f32 v[0:1], v[2:3], v[0:1]
	s_nop 0
	v_pk_add_f32 v[0:1], v[4:5], v[0:1]
	s_nop 0
	v_add_f32_e32 v0, v0, v1
	ds_bpermute_b32 v1, v148, v0
	s_waitcnt lgkmcnt(0)
	v_add_f32_e32 v0, v0, v1
	ds_bpermute_b32 v1, v149, v0
	s_waitcnt lgkmcnt(0)
	v_add_f32_e32 v0, v0, v1
	ds_bpermute_b32 v1, v150, v0
	s_waitcnt lgkmcnt(0)
	v_add_f32_e32 v0, v0, v1
	ds_bpermute_b32 v1, v151, v0
	s_waitcnt lgkmcnt(0)
	v_add_f32_e32 v0, v0, v1
	ds_bpermute_b32 v1, v152, v0
	s_waitcnt lgkmcnt(0)
	v_add_f32_e32 v0, v0, v1
	ds_bpermute_b32 v1, v153, v0
	s_waitcnt lgkmcnt(0)
	v_add_f32_e32 v0, v0, v1
	v_fmamk_f32 v0, v0, 0x3a000000, v91
	v_cmp_gt_f32_e32 vcc, s7, v0
	v_mul_f32_e32 v1, 0x4f800000, v0
	s_nop 0
	v_cndmask_b32_e32 v0, v0, v1, vcc
	v_sqrt_f32_e32 v1, v0
	s_nop 0
	v_add_u32_e32 v2, -1, v1
	v_fma_f32 v3, -v2, v1, v0
	v_cmp_ge_f32_e64 s[2:3], 0, v3
	v_add_u32_e32 v3, 1, v1
	s_nop 0
	v_cndmask_b32_e64 v2, v1, v2, s[2:3]
	v_fma_f32 v1, -v3, v1, v0
	v_cmp_lt_f32_e64 s[2:3], 0, v1
	s_nop 1
	v_cndmask_b32_e64 v1, v2, v3, s[2:3]
	v_mul_f32_e32 v2, 0x37800000, v1
	v_cndmask_b32_e32 v1, v1, v2, vcc
	v_cmp_class_f32_e32 vcc, v0, v92
	s_nop 1
	v_cndmask_b32_e32 v0, v1, v0, vcc
	v_div_scale_f32 v1, s[2:3], v0, v0, 1.0
	v_rcp_f32_e32 v2, v1
	s_add_i32 s2, s25, 4
	s_min_u32 s27, s2, 7
	s_or_b32 s2, s27, s4
	v_fma_f32 v3, -v1, v2, 1.0
	v_fmac_f32_e32 v2, v3, v2
	v_div_scale_f32 v3, vcc, 1.0, v0, 1.0
	v_mul_f32_e32 v4, v3, v2
	v_fma_f32 v5, -v1, v4, v3
	v_fmac_f32_e32 v4, v5, v2
	v_fma_f32 v1, -v1, v4, v3
	v_div_fmas_f32 v1, v1, v2, v4
	v_div_fixup_f32 v20, v1, v0, 1.0
	ds_read_b128 v[0:3], v89 offset:16384
	ds_read_b128 v[4:7], v89 offset:24576
	v_pk_mul_f32 v[22:23], v[44:45], v[20:21] op_sel_hi:[1,0]
	v_pk_mul_f32 v[40:41], v[42:43], v[20:21] op_sel_hi:[1,0]
	s_ashr_i32 s3, s2, 31
	v_pk_mul_f32 v[8:9], v[8:9], v[20:21] op_sel_hi:[1,0]
	s_waitcnt lgkmcnt(0)
	v_pk_fma_f32 v[2:3], v[2:3], v[40:41], v[6:7]
	v_pk_fma_f32 v[0:1], v[0:1], v[22:23], v[4:5]
	global_store_dwordx4 v[18:19], v[0:3], off offset:-4096
	ds_read_b128 v[0:3], v89 offset:17408
	ds_read_b128 v[4:7], v89 offset:25600
	v_pk_mul_f32 v[22:23], v[48:49], v[20:21] op_sel_hi:[1,0]
	v_pk_mul_f32 v[40:41], v[46:47], v[20:21] op_sel_hi:[1,0]
	v_pk_mul_f32 v[10:11], v[10:11], v[20:21] op_sel_hi:[1,0]
	s_lshl_b64 s[2:3], s[2:3], 12
	s_waitcnt lgkmcnt(0)
	v_pk_fma_f32 v[2:3], v[2:3], v[40:41], v[6:7]
	v_pk_fma_f32 v[0:1], v[0:1], v[22:23], v[4:5]
	global_store_dwordx4 v[18:19], v[0:3], off offset:-3072
	ds_read_b128 v[0:3], v89 offset:18432
	ds_read_b128 v[4:7], v89 offset:26624
	v_pk_mul_f32 v[22:23], v[56:57], v[20:21] op_sel_hi:[1,0]
	v_pk_mul_f32 v[40:41], v[54:55], v[20:21] op_sel_hi:[1,0]
	v_and_b32_e32 v47, 0xffff0000, v31
	v_lshlrev_b32_e32 v48, 16, v26
	s_waitcnt lgkmcnt(0)
	v_pk_fma_f32 v[2:3], v[2:3], v[40:41], v[6:7]
	v_pk_fma_f32 v[0:1], v[0:1], v[22:23], v[4:5]
	global_store_dwordx4 v[18:19], v[0:3], off offset:-2048
	ds_read_b128 v[0:3], v89 offset:19456
	ds_read_b128 v[4:7], v89 offset:27648
	v_pk_mul_f32 v[22:23], v[62:63], v[20:21] op_sel_hi:[1,0]
	v_pk_mul_f32 v[40:41], v[60:61], v[20:21] op_sel_hi:[1,0]
	v_lshlrev_b32_e32 v63, 16, v38
	v_lshlrev_b32_e32 v62, 16, v36
	s_waitcnt lgkmcnt(0)
	v_pk_fma_f32 v[2:3], v[2:3], v[40:41], v[6:7]
	v_pk_fma_f32 v[0:1], v[0:1], v[22:23], v[4:5]
	global_store_dwordx4 v[18:19], v[0:3], off offset:-1024
	ds_read_b128 v[0:3], v89 offset:20480
	ds_read_b128 v[4:7], v89 offset:28672
	v_pk_mul_f32 v[22:23], v[66:67], v[20:21] op_sel_hi:[1,0]
	v_pk_mul_f32 v[40:41], v[64:65], v[20:21] op_sel_hi:[1,0]
	v_and_b32_e32 v65, 0xffff0000, v38
	v_and_b32_e32 v64, 0xffff0000, v36
	s_waitcnt lgkmcnt(0)
	v_pk_fma_f32 v[2:3], v[2:3], v[40:41], v[6:7]
	v_pk_fma_f32 v[0:1], v[0:1], v[22:23], v[4:5]
	global_store_dwordx4 v[18:19], v[0:3], off
	ds_read_b128 v[0:3], v89 offset:21504
	ds_read_b128 v[4:7], v89 offset:29696
	v_pk_mul_f32 v[22:23], v[68:69], v[20:21] op_sel_hi:[1,0]
	v_pk_mul_f32 v[40:41], v[58:59], v[20:21] op_sel_hi:[1,0]
	v_lshlrev_b32_e32 v69, 16, v39
	v_lshlrev_b32_e32 v68, 16, v37
	s_waitcnt lgkmcnt(0)
	v_pk_fma_f32 v[2:3], v[2:3], v[40:41], v[6:7]
	v_pk_fma_f32 v[0:1], v[0:1], v[22:23], v[4:5]
	global_store_dwordx4 v[18:19], v[0:3], off offset:1024
	ds_read_b128 v[0:3], v89 offset:22528
	ds_read_b128 v[4:7], v89 offset:30720
	v_pk_mul_f32 v[22:23], v[74:75], v[20:21] op_sel_hi:[1,0]
	v_pk_mul_f32 v[40:41], v[72:73], v[20:21] op_sel_hi:[1,0]
	v_pk_add_f32 v[36:37], v[62:63], v[64:65]
	v_pk_add_f32 v[38:39], v[68:69], v[70:71]
	s_waitcnt lgkmcnt(0)
	v_pk_fma_f32 v[2:3], v[2:3], v[40:41], v[6:7]
	v_pk_fma_f32 v[0:1], v[0:1], v[22:23], v[4:5]
	global_store_dwordx4 v[18:19], v[0:3], off offset:2048
	ds_read_b128 v[0:3], v89 offset:23552
	ds_read_b128 v[4:7], v89 offset:31744
	v_lshl_add_u64 v[40:41], v[12:13], 0, s[2:3]
	s_lshl_b32 s2, s27, 4
	s_add_i32 s2, s19, s2
	v_pk_add_f32 v[36:37], v[36:37], v[38:39]
	s_waitcnt lgkmcnt(0)
	v_pk_fma_f32 v[0:1], v[0:1], v[10:11], v[4:5]
	v_pk_fma_f32 v[2:3], v[2:3], v[8:9], v[6:7]
	global_store_dwordx4 v[18:19], v[0:3], off offset:3072
	global_load_dwordx2 v[20:21], v[40:41], off
	global_load_dwordx2 v[22:23], v[40:41], off offset:512
	global_load_dwordx2 v[10:11], v[40:41], off offset:1024
	global_load_dwordx2 v[8:9], v[40:41], off offset:1536
	global_load_dwordx2 v[6:7], v[40:41], off offset:2048
	global_load_dwordx2 v[4:5], v[40:41], off offset:2560
	global_load_dwordx2 v[2:3], v[40:41], off offset:3072
	global_load_dwordx2 v[0:1], v[40:41], off offset:3584
	v_mov_b32_e32 v40, s2
	ds_read_b128 v[40:43], v40
	v_lshlrev_b32_e32 v61, 16, v35
	v_lshlrev_b32_e32 v60, 16, v34
	v_and_b32_e32 v35, 0xffff0000, v35
	v_and_b32_e32 v34, 0xffff0000, v34
	s_waitcnt lgkmcnt(0)
	v_readfirstlane_b32 s2, v40
	s_ashr_i32 s3, s2, 31
	s_lshl_b64 s[2:3], s[2:3], 11
	v_lshl_add_u64 v[44:45], v[14:15], 0, s[2:3]
	v_readfirstlane_b32 s2, v41
	s_ashr_i32 s3, s2, 31
	s_lshl_b64 s[2:3], s[2:3], 11
	v_lshl_add_u64 v[40:41], v[14:15], 0, s[2:3]
	v_readfirstlane_b32 s2, v42
	s_ashr_i32 s3, s2, 31
	s_lshl_b64 s[2:3], s[2:3], 11
	global_load_dword v82, v[44:45], off
	global_load_dword v109, v[44:45], off offset:256
	global_load_dword v105, v[44:45], off offset:512
	global_load_dword v101, v[44:45], off offset:768
	global_load_dword v66, v[44:45], off offset:1024
	global_load_dword v76, v[44:45], off offset:1280
	global_load_dword v72, v[44:45], off offset:1536
	global_load_dword v83, v[44:45], off offset:1792
	global_load_dword v113, v[40:41], off
	global_load_dword v110, v[40:41], off offset:256
	global_load_dword v106, v[40:41], off offset:512
	global_load_dword v102, v[40:41], off offset:768
	global_load_dword v84, v[40:41], off offset:1024
	global_load_dword v77, v[40:41], off offset:1280
	global_load_dword v73, v[40:41], off offset:1536
	global_load_dword v99, v[40:41], off offset:1792
	v_lshl_add_u64 v[40:41], v[14:15], 0, s[2:3]
	v_readfirstlane_b32 s2, v43
	s_ashr_i32 s3, s2, 31
	s_lshl_b64 s[2:3], s[2:3], 11
	global_load_dword v114, v[40:41], off
	global_load_dword v111, v[40:41], off offset:256
	global_load_dword v107, v[40:41], off offset:512
	global_load_dword v103, v[40:41], off offset:768
	global_load_dword v85, v[40:41], off offset:1024
	global_load_dword v78, v[40:41], off offset:1280
	global_load_dword v74, v[40:41], off offset:1536
	global_load_dword v81, v[40:41], off offset:1792
	v_lshl_add_u64 v[40:41], v[14:15], 0, s[2:3]
	global_load_dword v115, v[40:41], off
	global_load_dword v112, v[40:41], off offset:256
	global_load_dword v108, v[40:41], off offset:512
	global_load_dword v104, v[40:41], off offset:768
	global_load_dword v100, v[40:41], off offset:1024
	global_load_dword v80, v[40:41], off offset:1280
	global_load_dword v75, v[40:41], off offset:1536
	global_load_dword v79, v[40:41], off offset:1792
	ds_read_b128 v[40:43], v154 offset:256
	v_add_f32_e32 v36, 0, v36
	v_pk_add_f32 v[44:45], v[60:61], v[34:35]
	v_lshlrev_b32_e32 v38, 16, v33
	v_and_b32_e32 v39, 0xffff0000, v33
	s_waitcnt lgkmcnt(0)
	v_readfirstlane_b32 s30, v40
	v_readfirstlane_b32 s29, v41
	v_readfirstlane_b32 s27, v43
	v_add_f32_e32 v40, v36, v37
	v_lshlrev_b32_e32 v36, 16, v32
	v_and_b32_e32 v37, 0xffff0000, v32
	v_lshlrev_b32_e32 v41, 16, v30
	v_and_b32_e32 v43, 0xffff0000, v30
	v_lshlrev_b32_e32 v59, 16, v31
	v_pk_add_f32 v[30:31], v[44:45], v[44:45] op_sel:[0,1] op_sel_hi:[1,0]
	v_add_f32_e32 v58, v36, v37
	v_add_f32_e32 v46, v38, v39
	v_mov_b32_e32 v31, v43
	v_pk_add_f32 v[30:31], v[40:41], v[30:31]
	v_pk_add_f32 v[32:33], v[58:59], v[46:47]
	v_lshlrev_b32_e32 v45, 16, v29
	v_lshlrev_b32_e32 v44, 16, v28
	v_and_b32_e32 v29, 0xffff0000, v29
	v_and_b32_e32 v28, 0xffff0000, v28
	v_pk_add_f32 v[30:31], v[30:31], v[32:33]
	v_pk_add_f32 v[32:33], v[44:45], v[28:29]
	v_and_b32_e32 v49, 0xffff0000, v26
	v_lshlrev_b32_e32 v57, 16, v25
	v_and_b32_e32 v55, 0xffff0000, v25
	v_pk_add_f32 v[24:25], v[30:31], v[30:31] op_sel:[0,1] op_sel_hi:[1,0]
	v_pk_add_f32 v[26:27], v[32:33], v[32:33] op_sel:[0,1] op_sel_hi:[1,0]
	v_add_f32_e32 v56, v48, v49
	v_add_f32_e32 v54, v50, v51
	v_mov_b32_e32 v25, v52
	v_mov_b32_e32 v27, v53
	v_pk_add_f32 v[24:25], v[24:25], v[26:27]
	v_pk_add_f32 v[26:27], v[56:57], v[54:55]
	v_mul_f32_e32 v54, s30, v98
	v_pk_add_f32 v[24:25], v[24:25], v[26:27]
	v_mul_f32_e32 v154, s29, v98
	v_add_f32_e32 v24, v24, v25
	ds_bpermute_b32 v25, v148, v24
	v_readfirstlane_b32 s28, v42
	v_mul_f32_e32 v166, s27, v98
	v_lshl_add_u64 v[18:19], v[18:19], 0, s[20:21]
	s_waitcnt lgkmcnt(0)
	v_add_f32_e32 v24, v24, v25
	ds_bpermute_b32 v25, v149, v24
	s_waitcnt lgkmcnt(0)
	v_add_f32_e32 v24, v24, v25
	ds_bpermute_b32 v25, v150, v24
	s_waitcnt lgkmcnt(0)
	v_add_f32_e32 v24, v24, v25
	ds_bpermute_b32 v25, v151, v24
	s_waitcnt lgkmcnt(0)
	v_add_f32_e32 v24, v24, v25
	ds_bpermute_b32 v25, v152, v24
	s_waitcnt lgkmcnt(0)
	v_add_f32_e32 v24, v24, v25
	ds_bpermute_b32 v25, v153, v24
	s_waitcnt lgkmcnt(0)
	v_add_f32_e32 v40, v24, v25
	v_fmac_f32_e32 v70, 0xba000000, v40
	v_fmac_f32_e32 v64, 0xba000000, v40
	v_fmac_f32_e32 v71, 0xba000000, v40
	v_fmac_f32_e32 v65, 0xba000000, v40
	v_fmac_f32_e32 v68, 0xba000000, v40
	v_fmac_f32_e32 v62, 0xba000000, v40
	v_fmac_f32_e32 v69, 0xba000000, v40
	v_fmac_f32_e32 v63, 0xba000000, v40
	v_pk_mul_f32 v[24:25], v[64:65], v[64:65]
	v_pk_mul_f32 v[26:27], v[70:71], v[70:71]
	v_pk_fma_f32 v[24:25], v[62:63], v[62:63], v[24:25]
	v_pk_fma_f32 v[26:27], v[68:69], v[68:69], v[26:27]
	v_fmac_f32_e32 v34, 0xba000000, v40
	v_fmac_f32_e32 v35, 0xba000000, v40
	v_fmac_f32_e32 v61, 0xba000000, v40
	v_pk_add_f32 v[24:25], v[24:25], v[26:27]
	v_fmac_f32_e32 v60, 0xba000000, v40
	v_mov_b32_e32 v162, v61
	v_mov_b32_e32 v163, v35
	v_mov_b32_e32 v61, v34
	v_pk_add_f32 v[24:25], v[24:25], v[24:25] op_sel_hi:[0,1]
	v_pk_mul_f32 v[26:27], v[162:163], v[162:163]
	v_pk_mul_f32 v[30:31], v[60:61], v[60:61]
	v_fmac_f32_e32 v36, 0xba000000, v40
	v_pk_mov_b32 v[32:33], v[30:31], v[26:27] op_sel:[1,0]
	v_mov_b32_e32 v31, v27
	v_fmac_f32_e32 v37, 0xba000000, v40
	v_fmac_f32_e32 v38, 0xba000000, v40
	v_mul_f32_e32 v24, v36, v36
	v_pk_add_f32 v[26:27], v[32:33], v[30:31]
	v_fmac_f32_e32 v39, 0xba000000, v40
	v_pk_fma_f32 v[30:31], v[36:37], v[36:37], v[24:25] op_sel_hi:[1,1,0]
	v_mul_f32_e32 v24, v38, v38
	v_pk_add_f32 v[26:27], v[26:27], v[26:27] op_sel_hi:[0,1]
	v_pk_fma_f32 v[32:33], v[38:39], v[38:39], v[24:25] op_sel_hi:[1,1,0]
	v_fmac_f32_e32 v47, 0xba000000, v40
	v_fmac_f32_e32 v59, 0xba000000, v40
	v_fmac_f32_e32 v43, 0xba000000, v40
	v_fmac_f32_e32 v41, 0xba000000, v40
	v_mul_f32_e32 v30, v41, v41
	v_mul_f32_e32 v32, v43, v43
	v_mul_f32_e32 v26, v59, v59
	v_mul_f32_e32 v24, v47, v47
	v_pk_add_f32 v[30:31], v[30:31], v[32:33]
	v_pk_add_f32 v[24:25], v[26:27], v[24:25]
	v_fmac_f32_e32 v28, 0xba000000, v40
	v_fmac_f32_e32 v29, 0xba000000, v40
	v_fmac_f32_e32 v45, 0xba000000, v40
	v_mov_b32_e32 v156, v63
	v_mov_b32_e32 v158, v62
	v_pk_add_f32 v[24:25], v[30:31], v[24:25]
	v_fmac_f32_e32 v44, 0xba000000, v40
	v_mov_b32_e32 v62, v45
	v_mov_b32_e32 v63, v29
	v_mov_b32_e32 v45, v28
	v_pk_add_f32 v[24:25], v[24:25], v[24:25] op_sel_hi:[0,1]
	v_pk_mul_f32 v[26:27], v[62:63], v[62:63]
	v_pk_mul_f32 v[28:29], v[44:45], v[44:45]
	v_fmac_f32_e32 v48, 0xba000000, v40
	v_pk_mov_b32 v[30:31], v[28:29], v[26:27] op_sel:[1,0]
	v_mov_b32_e32 v29, v27
	v_fmac_f32_e32 v49, 0xba000000, v40
	v_fmac_f32_e32 v50, 0xba000000, v40
	v_mul_f32_e32 v24, v48, v48
	v_pk_add_f32 v[26:27], v[30:31], v[28:29]
	v_fmac_f32_e32 v51, 0xba000000, v40
	v_pk_fma_f32 v[28:29], v[48:49], v[48:49], v[24:25] op_sel_hi:[1,1,0]
	v_mul_f32_e32 v24, v50, v50
	v_pk_add_f32 v[26:27], v[26:27], v[26:27] op_sel_hi:[0,1]
	v_pk_fma_f32 v[30:31], v[50:51], v[50:51], v[24:25] op_sel_hi:[1,1,0]
	v_fmac_f32_e32 v55, 0xba000000, v40
	v_fmac_f32_e32 v57, 0xba000000, v40
	v_fmac_f32_e32 v53, 0xba000000, v40
	v_fmac_f32_e32 v52, 0xba000000, v40
	v_mul_f32_e32 v28, v52, v52
	v_mul_f32_e32 v30, v53, v53
	v_mul_f32_e32 v26, v57, v57
	v_mul_f32_e32 v24, v55, v55
	v_pk_add_f32 v[28:29], v[28:29], v[30:31]
	v_pk_add_f32 v[24:25], v[26:27], v[24:25]
	v_mov_b32_e32 v157, v65
	v_pk_add_f32 v[24:25], v[28:29], v[24:25]
	v_mov_b32_e32 v65, v71
	v_add_f32_e32 v24, v24, v25
	ds_bpermute_b32 v25, v148, v24
	v_mov_b32_e32 v161, v70
	v_cvt_pk_f32_fp8_sdwa v[70:71], v144 src0_sel:WORD_1
	v_mov_b32_e32 v159, v64
	v_mov_b32_e32 v64, v69
	s_waitcnt lgkmcnt(0)
	v_add_f32_e32 v24, v24, v25
	ds_bpermute_b32 v25, v149, v24
	v_mov_b32_e32 v160, v68
	v_cvt_pk_f32_fp8_e32 v[68:69], v144
	v_cvt_pk_f32_fp8_sdwa v[144:145], v145 src0_sel:WORD_1
	v_pk_fma_f32 v[70:71], v[54:55], v[70:71], 0 op_sel_hi:[0,1,0]
	s_waitcnt lgkmcnt(0)
	v_add_f32_e32 v24, v24, v25
	ds_bpermute_b32 v25, v150, v24
	v_pk_fma_f32 v[70:71], v[154:155], v[144:145], v[70:71] op_sel_hi:[0,1,1]
	s_waitcnt vmcnt(62)
	v_cvt_pk_f32_fp8_e32 v[144:145], v146
	v_pk_fma_f32 v[68:69], v[54:55], v[68:69], 0 op_sel_hi:[0,1,0]
	v_pk_fma_f32 v[68:69], v[154:155], v[164:165], v[68:69] op_sel_hi:[0,1,1]
	s_waitcnt lgkmcnt(0)
	v_add_f32_e32 v24, v24, v25
	ds_bpermute_b32 v25, v151, v24
	v_cvt_pk_f32_fp8_sdwa v[164:165], v146 src0_sel:WORD_1
	v_mul_f32_e32 v146, s28, v98
	s_waitcnt vmcnt(55)
	v_pk_fma_f32 v[68:69], v[146:147], v[144:145], v[68:69] op_sel_hi:[0,1,1]
	v_cvt_pk_f32_fp8_e32 v[144:145], v147
	s_waitcnt lgkmcnt(0)
	v_add_f32_e32 v24, v24, v25
	ds_bpermute_b32 v25, v152, v24
	v_pk_fma_f32 v[70:71], v[146:147], v[164:165], v[70:71] op_sel_hi:[0,1,1]
	v_pk_fma_f32 v[68:69], v[166:167], v[144:145], v[68:69] op_sel_hi:[0,1,1]
	v_cvt_pk_f32_fp8_sdwa v[164:165], v147 src0_sel:WORD_1
	v_mov_b32_e32 v46, v59
	s_waitcnt lgkmcnt(0)
	v_add_f32_e32 v24, v24, v25
	ds_bpermute_b32 v25, v153, v24
	v_pk_fma_f32 v[70:71], v[166:167], v[164:165], v[70:71] op_sel_hi:[0,1,1]
	v_mov_b32_e32 v42, v41
	s_waitcnt lgkmcnt(0)
	v_add_f32_e32 v24, v24, v25
	v_fmamk_f32 v24, v24, 0x3a000000, v91
	v_cmp_gt_f32_e32 vcc, s7, v24
	v_mul_f32_e32 v25, 0x4f800000, v24
	s_nop 0
	v_cndmask_b32_e32 v24, v24, v25, vcc
	v_sqrt_f32_e32 v25, v24
	s_nop 0
	v_add_u32_e32 v26, -1, v25
	v_fma_f32 v27, -v26, v25, v24
	v_cmp_ge_f32_e64 s[2:3], 0, v27
	v_add_u32_e32 v27, 1, v25
	s_nop 0
	v_cndmask_b32_e64 v26, v25, v26, s[2:3]
	v_fma_f32 v25, -v27, v25, v24
	v_cmp_lt_f32_e64 s[2:3], 0, v25
	s_nop 1
	v_cndmask_b32_e64 v25, v26, v27, s[2:3]
	v_mul_f32_e32 v26, 0x37800000, v25
	v_cndmask_b32_e32 v25, v25, v26, vcc
	v_cmp_class_f32_e32 vcc, v24, v92
	s_nop 1
	v_cndmask_b32_e32 v24, v25, v24, vcc
	v_div_scale_f32 v25, s[2:3], v24, v24, 1.0
	v_rcp_f32_e32 v26, v25
	s_nop 0
	v_fma_f32 v27, -v25, v26, 1.0
	v_fmac_f32_e32 v26, v27, v26
	v_div_scale_f32 v27, vcc, 1.0, v24, 1.0
	v_mul_f32_e32 v28, v27, v26
	v_fma_f32 v29, -v25, v28, v27
	v_fmac_f32_e32 v28, v29, v26
	v_fma_f32 v25, -v25, v28, v27
	v_div_fmas_f32 v25, v25, v26, v28
	v_div_fixup_f32 v56, v25, v24, 1.0
	ds_read_b128 v[24:27], v89
	ds_read_b128 v[28:31], v89 offset:8192
	ds_read_b128 v[32:35], v155 offset:32768
	v_pk_mul_f32 v[144:145], v[158:159], v[56:57] op_sel_hi:[1,0]
	v_pk_mul_f32 v[158:159], v[160:161], v[56:57] op_sel_hi:[1,0]
	v_cvt_pk_f32_fp8_e32 v[160:161], v141
	s_waitcnt lgkmcnt(1)
	v_pk_fma_f32 v[26:27], v[26:27], v[158:159], v[30:31]
	v_cvt_pk_f32_fp8_sdwa v[158:159], v140 src0_sel:WORD_1
	v_pk_fma_f32 v[24:25], v[24:25], v[144:145], v[28:29]
	v_cvt_pk_f32_fp8_e32 v[144:145], v140
	v_cvt_pk_f32_fp8_sdwa v[140:141], v141 src0_sel:WORD_1
	v_pk_fma_f32 v[158:159], v[54:55], v[158:159], 0 op_sel_hi:[0,1,0]
	v_pk_mul_f32 v[28:29], v[24:25], s[18:19] op_sel_hi:[1,0]
	v_pk_fma_f32 v[144:145], v[54:55], v[144:145], 0 op_sel_hi:[0,1,0]
	v_pk_fma_f32 v[140:141], v[154:155], v[140:141], v[158:159] op_sel_hi:[0,1,1]
	v_cvt_pk_f32_fp8_e32 v[158:159], v142
	v_pk_fma_f32 v[144:145], v[154:155], v[160:161], v[144:145] op_sel_hi:[0,1,1]
	v_cvt_pk_f32_fp8_sdwa v[160:161], v142 src0_sel:WORD_1
	v_pk_mul_f32 v[24:25], v[26:27], s[18:19] op_sel_hi:[1,0]
	v_pk_fma_f32 v[144:145], v[146:147], v[158:159], v[144:145] op_sel_hi:[0,1,1]
	s_waitcnt vmcnt(54)
	v_cvt_pk_f32_fp8_e32 v[158:159], v143
	v_cvt_pk_f32_fp8_sdwa v[142:143], v143 src0_sel:WORD_1
	s_waitcnt lgkmcnt(0)
	v_pk_fma_f32 v[24:25], v[34:35], v[70:71], v[24:25]
	v_pk_fma_f32 v[26:27], v[32:33], v[68:69], v[28:29]
	ds_read_b128 v[28:31], v89 offset:1024
	ds_read_b128 v[32:35], v89 offset:9216
	ds_read_b128 v[68:71], v155 offset:33792
	v_pk_fma_f32 v[140:141], v[146:147], v[160:161], v[140:141] op_sel_hi:[0,1,1]
	v_pk_fma_f32 v[140:141], v[166:167], v[142:143], v[140:141] op_sel_hi:[0,1,1]
	v_pk_mul_f32 v[142:143], v[156:157], v[56:57] op_sel_hi:[1,0]
	v_pk_mul_f32 v[64:65], v[64:65], v[56:57] op_sel_hi:[1,0]
	s_waitcnt lgkmcnt(1)
	v_pk_fma_f32 v[28:29], v[28:29], v[142:143], v[32:33]
	v_pk_fma_f32 v[144:145], v[166:167], v[158:159], v[144:145] op_sel_hi:[0,1,1]
	v_pk_fma_f32 v[30:31], v[30:31], v[64:65], v[34:35]
	v_pk_mul_f32 v[32:33], v[28:29], s[18:19] op_sel_hi:[1,0]
	v_pk_mul_f32 v[28:29], v[30:31], s[18:19] op_sel_hi:[1,0]
	s_waitcnt lgkmcnt(0)
	v_pk_fma_f32 v[30:31], v[68:69], v[144:145], v[32:33]
	v_pk_fma_f32 v[28:29], v[70:71], v[140:141], v[28:29]
	v_mov_b32_e32 v32, v30
	v_mov_b32_e32 v33, v26
	v_mov_b32_e32 v34, v31
	v_mov_b32_e32 v35, v27
	v_pk_add_f32 v[32:33], v[32:33], v[34:35]
	v_mov_b32_e32 v34, v28
	v_mov_b32_e32 v35, v24
	v_mov_b32_e32 v64, v29
	v_mov_b32_e32 v65, v25
	v_cvt_pk_f32_fp8_sdwa v[144:145], v136 src0_sel:WORD_1
	v_pk_add_f32 v[34:35], v[34:35], v[64:65]
	v_cvt_pk_f32_fp8_e32 v[64:65], v136
	v_cvt_pk_f32_fp8_e32 v[156:157], v137
	v_cvt_pk_f32_fp8_sdwa v[136:137], v137 src0_sel:WORD_1
	v_pk_fma_f32 v[144:145], v[54:55], v[144:145], 0 op_sel_hi:[0,1,0]
	v_pk_add_f32 v[32:33], v[32:33], v[34:35]
	v_pk_fma_f32 v[64:65], v[54:55], v[64:65], 0 op_sel_hi:[0,1,0]
	v_pk_fma_f32 v[136:137], v[154:155], v[136:137], v[144:145] op_sel_hi:[0,1,1]
	v_cvt_pk_f32_fp8_e32 v[144:145], v138
	v_add_f32_e32 v33, 0, v33
	v_pk_fma_f32 v[64:65], v[154:155], v[156:157], v[64:65] op_sel_hi:[0,1,1]
	v_cvt_pk_f32_fp8_sdwa v[156:157], v138 src0_sel:WORD_1
	v_add_f32_e32 v58, v32, v33
	ds_read_b128 v[32:35], v89 offset:2048
	ds_read_b128 v[68:71], v89 offset:10240
	ds_read_b128 v[140:143], v155 offset:34816
	v_pk_fma_f32 v[64:65], v[146:147], v[144:145], v[64:65] op_sel_hi:[0,1,1]
	s_waitcnt vmcnt(53)
	v_cvt_pk_f32_fp8_e32 v[144:145], v139
	v_cvt_pk_f32_fp8_sdwa v[138:139], v139 src0_sel:WORD_1
	v_pk_fma_f32 v[136:137], v[146:147], v[156:157], v[136:137] op_sel_hi:[0,1,1]
	v_pk_mul_f32 v[60:61], v[60:61], v[56:57] op_sel_hi:[1,0]
	v_pk_fma_f32 v[64:65], v[166:167], v[144:145], v[64:65] op_sel_hi:[0,1,1]
	v_pk_fma_f32 v[136:137], v[166:167], v[138:139], v[136:137] op_sel_hi:[0,1,1]
	v_pk_mul_f32 v[138:139], v[162:163], v[56:57] op_sel_hi:[1,0]
	s_waitcnt lgkmcnt(1)
	v_pk_fma_f32 v[60:61], v[32:33], v[60:61], v[68:69]
	v_pk_fma_f32 v[32:33], v[34:35], v[138:139], v[70:71]
	s_waitcnt lgkmcnt(0)
	v_pk_mul_f32 v[34:35], v[142:143], v[136:137]
	v_pk_mul_f32 v[64:65], v[140:141], v[64:65]
	v_pk_fma_f32 v[32:33], v[32:33], s[18:19], v[34:35] op_sel_hi:[1,0,1]
	v_pk_fma_f32 v[34:35], v[60:61], s[18:19], v[64:65] op_sel_hi:[1,0,1]
	v_mov_b32_e32 v65, v33
	v_pk_mov_b32 v[60:61], v[34:35], v[32:33] op_sel:[1,0]
	v_mov_b32_e32 v64, v34
	v_cvt_pk_f32_fp8_sdwa v[144:145], v132 src0_sel:WORD_1
	v_pk_add_f32 v[60:61], v[60:61], v[64:65]
	v_cvt_pk_f32_fp8_e32 v[64:65], v132
	v_cvt_pk_f32_fp8_e32 v[156:157], v133
	v_cvt_pk_f32_fp8_sdwa v[132:133], v133 src0_sel:WORD_1
	v_pk_fma_f32 v[144:145], v[54:55], v[144:145], 0 op_sel_hi:[0,1,0]
	v_pk_fma_f32 v[64:65], v[54:55], v[64:65], 0 op_sel_hi:[0,1,0]
	v_pk_fma_f32 v[64:65], v[154:155], v[156:157], v[64:65] op_sel_hi:[0,1,1]
	v_pk_fma_f32 v[132:133], v[154:155], v[132:133], v[144:145] op_sel_hi:[0,1,1]
	v_cvt_pk_f32_fp8_e32 v[144:145], v134
	v_cvt_pk_f32_fp8_sdwa v[156:157], v134 src0_sel:WORD_1
	ds_read_b128 v[68:71], v89 offset:3072
	ds_read_b128 v[136:139], v89 offset:11264
	ds_read_b128 v[140:143], v155 offset:35840
	v_pk_mul_f32 v[38:39], v[38:39], v[56:57] op_sel_hi:[1,0]
	v_pk_fma_f32 v[64:65], v[146:147], v[144:145], v[64:65] op_sel_hi:[0,1,1]
	s_waitcnt vmcnt(52)
	v_cvt_pk_f32_fp8_e32 v[144:145], v135
	v_cvt_pk_f32_fp8_sdwa v[134:135], v135 src0_sel:WORD_1
	v_pk_fma_f32 v[132:133], v[146:147], v[156:157], v[132:133] op_sel_hi:[0,1,1]
	v_pk_mul_f32 v[36:37], v[36:37], v[56:57] op_sel_hi:[1,0]
	v_pk_fma_f32 v[64:65], v[166:167], v[144:145], v[64:65] op_sel_hi:[0,1,1]
	v_pk_fma_f32 v[132:133], v[166:167], v[134:135], v[132:133] op_sel_hi:[0,1,1]
	v_cvt_pk_f32_fp8_sdwa v[144:145], v128 src0_sel:WORD_1
	s_waitcnt lgkmcnt(1)
	v_pk_fma_f32 v[68:69], v[36:37], v[68:69], v[136:137]
	v_pk_fma_f32 v[36:37], v[38:39], v[70:71], v[138:139]
	s_waitcnt lgkmcnt(0)
	v_pk_mul_f32 v[38:39], v[142:143], v[132:133]
	v_cvt_pk_f32_fp8_e32 v[142:143], v128
	v_cvt_pk_f32_fp8_e32 v[156:157], v129
	v_cvt_pk_f32_fp8_sdwa v[128:129], v129 src0_sel:WORD_1
	v_pk_fma_f32 v[144:145], v[54:55], v[144:145], 0 op_sel_hi:[0,1,0]
	v_pk_fma_f32 v[142:143], v[54:55], v[142:143], 0 op_sel_hi:[0,1,0]
	v_pk_mul_f32 v[64:65], v[140:141], v[64:65]
	v_pk_fma_f32 v[128:129], v[154:155], v[128:129], v[144:145] op_sel_hi:[0,1,1]
	v_cvt_pk_f32_fp8_e32 v[144:145], v130
	v_pk_fma_f32 v[142:143], v[154:155], v[156:157], v[142:143] op_sel_hi:[0,1,1]
	v_cvt_pk_f32_fp8_sdwa v[156:157], v130 src0_sel:WORD_1
	v_pk_fma_f32 v[36:37], v[36:37], s[18:19], v[38:39] op_sel_hi:[1,0,1]
	v_pk_fma_f32 v[38:39], v[68:69], s[18:19], v[64:65] op_sel_hi:[1,0,1]
	ds_read_b128 v[68:71], v89 offset:4096
	ds_read_b128 v[132:135], v89 offset:12288
	ds_read_b128 v[136:139], v155 offset:36864
	v_pk_fma_f32 v[142:143], v[146:147], v[144:145], v[142:143] op_sel_hi:[0,1,1]
	s_waitcnt vmcnt(51)
	v_cvt_pk_f32_fp8_e32 v[144:145], v131
	v_cvt_pk_f32_fp8_sdwa v[130:131], v131 src0_sel:WORD_1
	v_pk_fma_f32 v[128:129], v[146:147], v[156:157], v[128:129] op_sel_hi:[0,1,1]
	v_pk_mul_f32 v[46:47], v[46:47], v[56:57] op_sel_hi:[1,0]
	v_pk_fma_f32 v[142:143], v[166:167], v[144:145], v[142:143] op_sel_hi:[0,1,1]
	v_pk_fma_f32 v[128:129], v[166:167], v[130:131], v[128:129] op_sel_hi:[0,1,1]
	v_pk_mul_f32 v[40:41], v[42:43], v[56:57] op_sel_hi:[1,0]
	v_pk_add_f32 v[60:61], v[60:61], v[60:61] op_sel:[0,1] op_sel_hi:[1,0]
	s_waitcnt lgkmcnt(1)
	v_pk_fma_f32 v[42:43], v[40:41], v[68:69], v[132:133]
	v_pk_fma_f32 v[40:41], v[46:47], v[70:71], v[134:135]
	s_waitcnt lgkmcnt(0)
	v_pk_mul_f32 v[46:47], v[138:139], v[128:129]
	v_pk_mul_f32 v[68:69], v[136:137], v[142:143]
	v_pk_fma_f32 v[40:41], v[40:41], s[18:19], v[46:47] op_sel_hi:[1,0,1]
	v_pk_fma_f32 v[42:43], v[42:43], s[18:19], v[68:69] op_sel_hi:[1,0,1]
	v_add_f32_e32 v64, v38, v39
	v_add_f32_e32 v140, v36, v37
	v_mov_b32_e32 v59, v42
	v_mov_b32_e32 v61, v43
	v_mov_b32_e32 v65, v40
	v_mov_b32_e32 v141, v41
	v_pk_add_f32 v[46:47], v[58:59], v[60:61]
	v_pk_add_f32 v[58:59], v[64:65], v[140:141]
	v_cvt_pk_f32_fp8_sdwa v[64:65], v124 src0_sel:WORD_1
	v_pk_add_f32 v[46:47], v[46:47], v[58:59]
	v_cvt_pk_f32_fp8_e32 v[134:135], v125
	v_pk_add_f32 v[132:133], v[46:47], v[46:47] op_sel:[0,1] op_sel_hi:[1,0]
	v_cvt_pk_f32_fp8_e32 v[46:47], v124
	v_cvt_pk_f32_fp8_sdwa v[124:125], v125 src0_sel:WORD_1
	v_pk_fma_f32 v[64:65], v[54:55], v[64:65], 0 op_sel_hi:[0,1,0]
	ds_read_b128 v[58:61], v89 offset:5120
	ds_read_b128 v[68:71], v89 offset:13312
	ds_read_b128 v[128:131], v155 offset:37888
	v_pk_fma_f32 v[46:47], v[54:55], v[46:47], 0 op_sel_hi:[0,1,0]
	v_pk_fma_f32 v[64:65], v[154:155], v[124:125], v[64:65] op_sel_hi:[0,1,1]
	v_cvt_pk_f32_fp8_e32 v[124:125], v126
	v_pk_fma_f32 v[46:47], v[154:155], v[134:135], v[46:47] op_sel_hi:[0,1,1]
	v_cvt_pk_f32_fp8_sdwa v[134:135], v126 src0_sel:WORD_1
	v_pk_mul_f32 v[62:63], v[62:63], v[56:57] op_sel_hi:[1,0]
	v_pk_fma_f32 v[46:47], v[146:147], v[124:125], v[46:47] op_sel_hi:[0,1,1]
	s_waitcnt vmcnt(50)
	v_cvt_pk_f32_fp8_e32 v[124:125], v127
	v_cvt_pk_f32_fp8_sdwa v[126:127], v127 src0_sel:WORD_1
	v_pk_fma_f32 v[64:65], v[146:147], v[134:135], v[64:65] op_sel_hi:[0,1,1]
	v_pk_mul_f32 v[44:45], v[44:45], v[56:57] op_sel_hi:[1,0]
	v_pk_fma_f32 v[46:47], v[166:167], v[124:125], v[46:47] op_sel_hi:[0,1,1]
	v_pk_fma_f32 v[64:65], v[166:167], v[126:127], v[64:65] op_sel_hi:[0,1,1]
	s_waitcnt lgkmcnt(0)
	v_pk_mul_f32 v[46:47], v[128:129], v[46:47]
	v_cvt_pk_f32_fp8_sdwa v[128:129], v120 src0_sel:WORD_1
	v_pk_fma_f32 v[58:59], v[44:45], v[58:59], v[68:69]
	v_pk_fma_f32 v[44:45], v[62:63], v[60:61], v[70:71]
	v_pk_mul_f32 v[60:61], v[130:131], v[64:65]
	v_cvt_pk_f32_fp8_e32 v[126:127], v120
	v_cvt_pk_f32_fp8_e32 v[130:131], v121
	v_cvt_pk_f32_fp8_sdwa v[120:121], v121 src0_sel:WORD_1
	v_pk_fma_f32 v[128:129], v[54:55], v[128:129], 0 op_sel_hi:[0,1,0]
	v_pk_fma_f32 v[44:45], v[44:45], s[18:19], v[60:61] op_sel_hi:[1,0,1]
	v_pk_fma_f32 v[46:47], v[58:59], s[18:19], v[46:47] op_sel_hi:[1,0,1]
	v_pk_fma_f32 v[120:121], v[154:155], v[120:121], v[128:129] op_sel_hi:[0,1,1]
	v_cvt_pk_f32_fp8_e32 v[128:129], v122
	v_pk_mov_b32 v[58:59], v[46:47], v[44:45] op_sel:[1,0]
	v_mov_b32_e32 v60, v46
	v_mov_b32_e32 v61, v45
	v_pk_fma_f32 v[126:127], v[54:55], v[126:127], 0 op_sel_hi:[0,1,0]
	v_pk_add_f32 v[58:59], v[58:59], v[60:61]
	v_pk_fma_f32 v[126:127], v[154:155], v[130:131], v[126:127] op_sel_hi:[0,1,1]
	v_pk_add_f32 v[124:125], v[58:59], v[58:59] op_sel:[0,1] op_sel_hi:[1,0]
	ds_read_b128 v[58:61], v89 offset:6144
	ds_read_b128 v[62:65], v89 offset:14336
	ds_read_b128 v[68:71], v155 offset:38912
	v_pk_fma_f32 v[126:127], v[146:147], v[128:129], v[126:127] op_sel_hi:[0,1,1]
	s_waitcnt vmcnt(49)
	v_cvt_pk_f32_fp8_e32 v[128:129], v123
	v_cvt_pk_f32_fp8_sdwa v[130:131], v122 src0_sel:WORD_1
	v_pk_mul_f32 v[50:51], v[50:51], v[56:57] op_sel_hi:[1,0]
	v_pk_mul_f32 v[48:49], v[48:49], v[56:57] op_sel_hi:[1,0]
	v_pk_fma_f32 v[126:127], v[166:167], v[128:129], v[126:127] op_sel_hi:[0,1,1]
	v_cvt_pk_f32_fp8_sdwa v[128:129], v116 src0_sel:WORD_1
	v_pk_fma_f32 v[120:121], v[146:147], v[130:131], v[120:121] op_sel_hi:[0,1,1]
	s_waitcnt lgkmcnt(1)
	v_pk_fma_f32 v[58:59], v[48:49], v[58:59], v[62:63]
	v_pk_fma_f32 v[48:49], v[50:51], v[60:61], v[64:65]
	s_waitcnt lgkmcnt(0)
	v_pk_mul_f32 v[60:61], v[68:69], v[126:127]
	v_cvt_pk_f32_fp8_e32 v[126:127], v116
	v_cvt_pk_f32_fp8_e32 v[130:131], v117
	v_cvt_pk_f32_fp8_sdwa v[116:117], v117 src0_sel:WORD_1
	v_cvt_pk_f32_fp8_sdwa v[122:123], v123 src0_sel:WORD_1
	v_pk_fma_f32 v[128:129], v[54:55], v[128:129], 0 op_sel_hi:[0,1,0]
	v_pk_fma_f32 v[126:127], v[54:55], v[126:127], 0 op_sel_hi:[0,1,0]
	v_pk_fma_f32 v[116:117], v[154:155], v[116:117], v[128:129] op_sel_hi:[0,1,1]
	v_cvt_pk_f32_fp8_e32 v[128:129], v118
	v_pk_fma_f32 v[120:121], v[166:167], v[122:123], v[120:121] op_sel_hi:[0,1,1]
	v_pk_mul_f32 v[50:51], v[70:71], v[120:121]
	v_pk_fma_f32 v[126:127], v[154:155], v[130:131], v[126:127] op_sel_hi:[0,1,1]
	v_cvt_pk_f32_fp8_sdwa v[130:131], v118 src0_sel:WORD_1
	v_pk_fma_f32 v[48:49], v[48:49], s[18:19], v[50:51] op_sel_hi:[1,0,1]
	v_pk_fma_f32 v[50:51], v[58:59], s[18:19], v[60:61] op_sel_hi:[1,0,1]
	ds_read_b128 v[58:61], v89 offset:7168
	ds_read_b128 v[62:65], v89 offset:15360
	ds_read_b128 v[68:71], v155 offset:39936
	v_pk_fma_f32 v[126:127], v[146:147], v[128:129], v[126:127] op_sel_hi:[0,1,1]
	s_waitcnt vmcnt(48)
	v_cvt_pk_f32_fp8_e32 v[128:129], v119
	v_cvt_pk_f32_fp8_sdwa v[118:119], v119 src0_sel:WORD_1
	v_pk_fma_f32 v[116:117], v[146:147], v[130:131], v[116:117] op_sel_hi:[0,1,1]
	v_mov_b32_e32 v54, v57
	v_pk_fma_f32 v[126:127], v[166:167], v[128:129], v[126:127] op_sel_hi:[0,1,1]
	v_pk_fma_f32 v[116:117], v[166:167], v[118:119], v[116:117] op_sel_hi:[0,1,1]
	v_pk_mul_f32 v[54:55], v[54:55], v[56:57] op_sel_hi:[1,0]
	v_pk_mul_f32 v[52:53], v[52:53], v[56:57] op_sel_hi:[1,0]
	s_waitcnt lgkmcnt(1)
	v_pk_fma_f32 v[54:55], v[54:55], v[60:61], v[64:65]
	v_pk_fma_f32 v[52:53], v[52:53], v[58:59], v[62:63]
	s_waitcnt lgkmcnt(0)
	v_pk_mul_f32 v[56:57], v[70:71], v[116:117]
	v_pk_mul_f32 v[58:59], v[68:69], v[126:127]
	v_pk_fma_f32 v[54:55], v[54:55], s[18:19], v[56:57] op_sel_hi:[1,0,1]
	v_pk_fma_f32 v[52:53], v[52:53], s[18:19], v[58:59] op_sel_hi:[1,0,1]
	v_add_f32_e32 v120, v50, v51
	v_add_f32_e32 v122, v48, v49
	v_mov_b32_e32 v133, v52
	v_mov_b32_e32 v125, v53
	v_mov_b32_e32 v121, v54
	v_mov_b32_e32 v123, v55
	v_pk_add_f32 v[56:57], v[132:133], v[124:125]
	v_pk_add_f32 v[58:59], v[120:121], v[122:123]
	s_nop 0
	v_pk_add_f32 v[56:57], v[56:57], v[58:59]
	s_nop 0
	v_add_f32_e32 v56, v56, v57
	ds_bpermute_b32 v57, v148, v56
	s_waitcnt lgkmcnt(0)
	v_add_f32_e32 v56, v56, v57
	ds_bpermute_b32 v57, v149, v56
	s_waitcnt lgkmcnt(0)
	v_add_f32_e32 v56, v56, v57
	ds_bpermute_b32 v57, v150, v56
	s_waitcnt lgkmcnt(0)
	v_add_f32_e32 v56, v56, v57
	ds_bpermute_b32 v57, v151, v56
	s_waitcnt lgkmcnt(0)
	v_add_f32_e32 v56, v56, v57
	ds_bpermute_b32 v57, v152, v56
	s_waitcnt lgkmcnt(0)
	v_add_f32_e32 v56, v56, v57
	ds_bpermute_b32 v57, v153, v56
	s_waitcnt lgkmcnt(0)
	v_add_f32_e32 v64, v56, v57
	v_fmamk_f32 v27, v64, 0xba000000, v27
	v_fmamk_f32 v31, v64, 0xba000000, v31
	v_fmamk_f32 v25, v64, 0xba000000, v25
	v_fmac_f32_e32 v26, 0xba000000, v64
	v_fmamk_f32 v29, v64, 0xba000000, v29
	v_fmac_f32_e32 v30, 0xba000000, v64
	v_mov_b32_e32 v58, v27
	v_mov_b32_e32 v59, v31
	v_fmac_f32_e32 v24, 0xba000000, v64
	v_fmac_f32_e32 v28, 0xba000000, v64
	v_mov_b32_e32 v56, v26
	v_mov_b32_e32 v57, v30
	v_pk_mul_f32 v[58:59], v[58:59], v[58:59]
	v_mov_b32_e32 v60, v25
	v_mov_b32_e32 v61, v29
	v_pk_fma_f32 v[56:57], v[56:57], v[56:57], v[58:59]
	v_mov_b32_e32 v58, v24
	v_mov_b32_e32 v59, v28
	v_pk_mul_f32 v[60:61], v[60:61], v[60:61]
	v_fmamk_f32 v35, v64, 0xba000000, v35
	v_pk_fma_f32 v[58:59], v[58:59], v[58:59], v[60:61]
	v_fmac_f32_e32 v34, 0xba000000, v64
	v_pk_add_f32 v[56:57], v[56:57], v[58:59]
	v_fmamk_f32 v33, v64, 0xba000000, v33
	v_fmac_f32_e32 v32, 0xba000000, v64
	v_pk_add_f32 v[56:57], v[56:57], v[56:57] op_sel_hi:[0,1]
	v_pk_mul_f32 v[58:59], v[32:33], v[32:33]
	v_pk_mul_f32 v[60:61], v[34:35], v[34:35]
	v_fmac_f32_e32 v38, 0xba000000, v64
	v_pk_mov_b32 v[62:63], v[60:61], v[58:59] op_sel:[1,0]
	v_mov_b32_e32 v61, v59
	v_fmamk_f32 v39, v64, 0xba000000, v39
	v_fmac_f32_e32 v36, 0xba000000, v64
	v_mul_f32_e32 v56, v38, v38
	v_pk_add_f32 v[58:59], v[62:63], v[60:61]
	v_fmamk_f32 v37, v64, 0xba000000, v37
	v_pk_fma_f32 v[60:61], v[38:39], v[38:39], v[56:57] op_sel_hi:[1,1,0]
	v_mul_f32_e32 v56, v36, v36
	v_pk_add_f32 v[58:59], v[58:59], v[58:59] op_sel_hi:[0,1]
	v_pk_fma_f32 v[62:63], v[36:37], v[36:37], v[56:57] op_sel_hi:[1,1,0]
	v_fmamk_f32 v41, v64, 0xba000000, v41
	v_fmac_f32_e32 v40, 0xba000000, v64
	v_fmamk_f32 v43, v64, 0xba000000, v43
	v_fmac_f32_e32 v42, 0xba000000, v64
	v_mul_f32_e32 v60, v42, v42
	v_mul_f32_e32 v62, v43, v43
	v_mul_f32_e32 v58, v40, v40
	v_mul_f32_e32 v56, v41, v41
	v_pk_add_f32 v[60:61], v[60:61], v[62:63]
	v_pk_add_f32 v[56:57], v[58:59], v[56:57]
	v_fmamk_f32 v47, v64, 0xba000000, v47
	v_pk_add_f32 v[56:57], v[60:61], v[56:57]
	v_fmac_f32_e32 v46, 0xba000000, v64
	v_fmamk_f32 v45, v64, 0xba000000, v45
	v_fmac_f32_e32 v44, 0xba000000, v64
	v_pk_add_f32 v[56:57], v[56:57], v[56:57] op_sel_hi:[0,1]
	v_pk_mul_f32 v[58:59], v[44:45], v[44:45]
	v_pk_mul_f32 v[60:61], v[46:47], v[46:47]
	v_fmac_f32_e32 v50, 0xba000000, v64
	v_pk_mov_b32 v[62:63], v[60:61], v[58:59] op_sel:[1,0]
	v_mov_b32_e32 v61, v59
	v_fmamk_f32 v51, v64, 0xba000000, v51
	v_fmac_f32_e32 v48, 0xba000000, v64
	v_mul_f32_e32 v56, v50, v50
	v_pk_add_f32 v[58:59], v[62:63], v[60:61]
	v_fmamk_f32 v49, v64, 0xba000000, v49
	v_pk_fma_f32 v[60:61], v[50:51], v[50:51], v[56:57] op_sel_hi:[1,1,0]
	v_mul_f32_e32 v56, v48, v48
	v_pk_add_f32 v[58:59], v[58:59], v[58:59] op_sel_hi:[0,1]
	v_pk_fma_f32 v[62:63], v[48:49], v[48:49], v[56:57] op_sel_hi:[1,1,0]
	v_fmamk_f32 v55, v64, 0xba000000, v55
	v_fmac_f32_e32 v54, 0xba000000, v64
	v_fmamk_f32 v53, v64, 0xba000000, v53
	v_fmac_f32_e32 v52, 0xba000000, v64
	v_mul_f32_e32 v60, v52, v52
	v_mul_f32_e32 v62, v53, v53
	v_mul_f32_e32 v58, v54, v54
	v_mul_f32_e32 v56, v55, v55
	v_pk_add_f32 v[60:61], v[60:61], v[62:63]
	v_pk_add_f32 v[56:57], v[58:59], v[56:57]
	s_nop 0
	v_pk_add_f32 v[56:57], v[60:61], v[56:57]
	s_nop 0
	v_add_f32_e32 v56, v56, v57
	ds_bpermute_b32 v57, v148, v56
	s_waitcnt lgkmcnt(0)
	v_add_f32_e32 v56, v56, v57
	ds_bpermute_b32 v57, v149, v56
	s_waitcnt lgkmcnt(0)
	v_add_f32_e32 v56, v56, v57
	ds_bpermute_b32 v57, v150, v56
	s_waitcnt lgkmcnt(0)
	v_add_f32_e32 v56, v56, v57
	ds_bpermute_b32 v57, v151, v56
	s_waitcnt lgkmcnt(0)
	v_add_f32_e32 v56, v56, v57
	ds_bpermute_b32 v57, v152, v56
	s_waitcnt lgkmcnt(0)
	v_add_f32_e32 v56, v56, v57
	ds_bpermute_b32 v57, v153, v56
	s_waitcnt lgkmcnt(0)
	v_add_f32_e32 v56, v56, v57
	v_fmamk_f32 v56, v56, 0x3a000000, v91
	v_cmp_gt_f32_e32 vcc, s7, v56
	v_mul_f32_e32 v57, 0x4f800000, v56
	s_nop 0
	v_cndmask_b32_e32 v56, v56, v57, vcc
	v_sqrt_f32_e32 v57, v56
	s_nop 0
	v_add_u32_e32 v58, -1, v57
	v_fma_f32 v59, -v58, v57, v56
	v_cmp_ge_f32_e64 s[2:3], 0, v59
	v_add_u32_e32 v59, 1, v57
	s_nop 0
	v_cndmask_b32_e64 v58, v57, v58, s[2:3]
	v_fma_f32 v57, -v59, v57, v56
	v_cmp_lt_f32_e64 s[2:3], 0, v57
	s_nop 1
	v_cndmask_b32_e64 v57, v58, v59, s[2:3]
	v_mul_f32_e32 v58, 0x37800000, v57
	v_cndmask_b32_e32 v57, v57, v58, vcc
	v_cmp_class_f32_e32 vcc, v56, v92
	s_nop 1
	v_cndmask_b32_e32 v56, v57, v56, vcc
	v_div_scale_f32 v57, s[2:3], v56, v56, 1.0
	v_rcp_f32_e32 v58, v57
	s_lshl_b64 s[2:3], s[22:23], 13
	s_add_u32 s2, s8, s2
	s_addc_u32 s3, s9, s3
	v_fma_f32 v59, -v57, v58, 1.0
	v_fmac_f32_e32 v58, v59, v58
	v_div_scale_f32 v59, vcc, 1.0, v56, 1.0
	v_mul_f32_e32 v60, v59, v58
	v_fma_f32 v61, -v57, v60, v59
	v_fmac_f32_e32 v60, v61, v58
	v_fma_f32 v57, -v57, v60, v59
	v_div_fmas_f32 v57, v57, v58, v60
	ds_read_b128 v[58:61], v89 offset:16384
	ds_read_b128 v[62:65], v89 offset:24576
	v_div_fixup_f32 v56, v57, v56, 1.0
	v_pk_mul_f32 v[68:69], v[26:27], v[56:57] op_sel_hi:[1,0]
	v_pk_mul_f32 v[24:25], v[24:25], v[56:57] op_sel_hi:[1,0]
	v_pk_mul_f32 v[30:31], v[30:31], v[56:57] op_sel_hi:[1,0]
	s_waitcnt lgkmcnt(0)
	v_pk_fma_f32 v[26:27], v[60:61], v[24:25], v[64:65]
	v_pk_fma_f32 v[24:25], v[58:59], v[68:69], v[62:63]
	global_store_dwordx4 v93, v[24:27], s[2:3] nt
	ds_read_b128 v[24:27], v89 offset:17408
	ds_read_b128 v[58:61], v89 offset:25600
	v_pk_mul_f32 v[28:29], v[28:29], v[56:57] op_sel_hi:[1,0]
	v_pk_mul_f32 v[34:35], v[34:35], v[56:57] op_sel_hi:[1,0]
	v_pk_mul_f32 v[32:33], v[32:33], v[56:57] op_sel_hi:[1,0]
	s_add_i32 s25, s25, 2
	s_waitcnt lgkmcnt(0)
	v_pk_fma_f32 v[26:27], v[26:27], v[28:29], v[60:61]
	v_pk_fma_f32 v[24:25], v[24:25], v[30:31], v[58:59]
	global_store_dwordx4 v93, v[24:27], s[2:3] offset:1024 nt
	ds_read_b128 v[24:27], v89 offset:18432
	ds_read_b128 v[28:31], v89 offset:26624
	s_add_i32 s26, s26, 32
	s_cmp_gt_u32 s25, 5
	s_waitcnt lgkmcnt(0)
	v_pk_fma_f32 v[26:27], v[26:27], v[32:33], v[30:31]
	v_pk_fma_f32 v[24:25], v[24:25], v[34:35], v[28:29]
	global_store_dwordx4 v93, v[24:27], s[2:3] offset:2048 nt
	ds_read_b128 v[24:27], v89 offset:19456
	ds_read_b128 v[28:31], v89 offset:27648
	v_pk_mul_f32 v[32:33], v[38:39], v[56:57] op_sel_hi:[1,0]
	v_pk_mul_f32 v[34:35], v[36:37], v[56:57] op_sel_hi:[1,0]
	s_waitcnt lgkmcnt(0)
	v_pk_fma_f32 v[24:25], v[24:25], v[32:33], v[28:29]
	v_pk_fma_f32 v[26:27], v[26:27], v[34:35], v[30:31]
	global_store_dwordx4 v93, v[24:27], s[2:3] offset:3072 nt
	ds_read_b128 v[24:27], v89 offset:20480
	ds_read_b128 v[28:31], v89 offset:28672
	v_pk_mul_f32 v[32:33], v[42:43], v[56:57] op_sel_hi:[1,0]
	v_pk_mul_f32 v[34:35], v[40:41], v[56:57] op_sel_hi:[1,0]
	s_waitcnt lgkmcnt(0)
	v_pk_fma_f32 v[24:25], v[24:25], v[32:33], v[28:29]
	v_pk_fma_f32 v[26:27], v[26:27], v[34:35], v[30:31]
	global_store_dwordx4 v94, v[24:27], s[2:3] nt
	ds_read_b128 v[24:27], v89 offset:21504
	ds_read_b128 v[28:31], v89 offset:29696
	v_pk_mul_f32 v[32:33], v[46:47], v[56:57] op_sel_hi:[1,0]
	v_pk_mul_f32 v[34:35], v[44:45], v[56:57] op_sel_hi:[1,0]
	s_waitcnt lgkmcnt(0)
	v_pk_fma_f32 v[24:25], v[24:25], v[32:33], v[28:29]
	v_pk_fma_f32 v[26:27], v[26:27], v[34:35], v[30:31]
	global_store_dwordx4 v95, v[24:27], s[2:3] nt
	ds_read_b128 v[24:27], v89 offset:22528
	ds_read_b128 v[28:31], v89 offset:30720
	v_pk_mul_f32 v[32:33], v[50:51], v[56:57] op_sel_hi:[1,0]
	v_pk_mul_f32 v[34:35], v[48:49], v[56:57] op_sel_hi:[1,0]
	s_waitcnt lgkmcnt(0)
	v_pk_fma_f32 v[24:25], v[24:25], v[32:33], v[28:29]
	v_pk_fma_f32 v[26:27], v[26:27], v[34:35], v[30:31]
	global_store_dwordx4 v96, v[24:27], s[2:3] nt
	ds_read_b128 v[24:27], v89 offset:23552
	ds_read_b128 v[28:31], v89 offset:31744
	v_pk_mul_f32 v[32:33], v[54:55], v[56:57] op_sel_hi:[1,0]
	v_pk_mul_f32 v[34:35], v[52:53], v[56:57] op_sel_hi:[1,0]
	s_waitcnt lgkmcnt(0)
	v_pk_fma_f32 v[26:27], v[26:27], v[32:33], v[30:31]
	v_pk_fma_f32 v[24:25], v[24:25], v[34:35], v[28:29]
	global_store_dwordx4 v97, v[24:27], s[2:3] nt
	s_cbranch_scc0 .LBB0_1515
	s_waitcnt lgkmcnt(0)
	s_add_i32 s4, s4, s6
	s_cmpk_gt_i32 s4, 0x3fff
	v_lshl_add_u64 v[16:17], v[16:17], 0, s[16:17]
	s_cbranch_scc0 .LBB0_1512
